# SCAN1 (RWKV chunk pass): packed f32 VALU ops split into scalar pairs (bit-identical); on top of v35
# speedup vs baseline: 1.0041x; 1.0041x over previous
.LBB0_1289:
	s_or_b64 exec, exec, s[0:1]
	v_lshlrev_b32_e32 v214, 3, v212
	s_waitcnt lgkmcnt(0)
	v_add_u32_e32 v216, s36, v214
	v_add_u32_e32 v130, 0x3c00, v216
	ds_read_b64_tr_b16 v[132:133], v130
	v_add_u32_e32 v130, 0x3e00, v216
	ds_read_b64_tr_b16 v[170:171], v130
	v_add_u32_e32 v130, 0x800, v216
	ds_read_b64_tr_b16 v[148:149], v130
	v_add_u32_e32 v130, 0xa00, v216
	ds_read_b64_tr_b16 v[150:151], v130
	v_add_u32_e32 v130, 0x3000, v216
	ds_read_b64_tr_b16 v[136:137], v216
	ds_read_b64_tr_b16 v[142:143], v130
	v_add_u32_e32 v130, 0x200, v216
	ds_read_b64_tr_b16 v[140:141], v130
	v_add_u32_e32 v130, 0x3200, v216
	ds_read_b64_tr_b16 v[138:139], v130
	v_add_u32_e32 v130, 0x400, v216
	ds_read_b64_tr_b16 v[172:173], v130
	v_add_u32_e32 v130, 0x3400, v216
	ds_read_b64_tr_b16 v[134:135], v130
	v_add_u32_e32 v130, 0x600, v216
	ds_read_b64_tr_b16 v[174:175], v130
	v_add_u32_e32 v130, 0x3600, v216
	ds_read_b64_tr_b16 v[130:131], v130
	s_waitcnt lgkmcnt(0)
	v_mfma_f32_16x16x16_f16 v[156:159], v[170:171], v[142:143], 0
	v_mfma_f32_16x16x16_f16 v[152:155], v[132:133], v[136:137], 0
	v_mfma_f32_16x16x16_f16 v[166:169], v[170:171], v[138:139], 0
	s_nop 5
	v_cvt_pk_f16_f32 v137, v158, v159
	v_cvt_pk_f16_f32 v136, v156, v157
	v_cvt_pk_f16_f32 v203, v154, v155
	v_cvt_pk_f16_f32 v202, v152, v153
	v_mfma_f32_16x16x16_f16 v[156:159], v[132:133], v[136:137], 0
	v_cvt_pk_f16_f32 v137, v168, v169
	v_cvt_pk_f16_f32 v136, v166, v167
	v_mfma_f32_16x16x16_f16 v[152:155], v[132:133], v[172:173], 0
	s_nop 0
	v_mfma_f32_16x16x16_f16 v[166:169], v[132:133], v[136:137], 0
	s_nop 2
	v_cvt_pk_f16_f32 v147, v158, v159
	v_cvt_pk_f16_f32 v146, v156, v157
	s_nop 0
	v_cvt_pk_f16_f32 v199, v154, v155
	v_mfma_f32_16x16x16_f16 v[156:159], v[170:171], v[134:135], 0
	v_cvt_pk_f16_f32 v198, v152, v153
	v_mfma_f32_16x16x16_f16 v[152:155], v[132:133], v[174:175], 0
	v_mfma_f32_16x16x16_f16 v[162:165], v[132:133], v[140:141], 0
	s_nop 4
	v_cvt_pk_f16_f32 v137, v158, v159
	v_cvt_pk_f16_f32 v136, v156, v157
	v_cvt_pk_f16_f32 v197, v154, v155
	v_cvt_pk_f16_f32 v196, v152, v153
	v_mfma_f32_16x16x16_f16 v[156:159], v[132:133], v[136:137], 0
	v_cvt_pk_f16_f32 v200, v162, v163
	v_cvt_pk_f16_f32 v201, v164, v165
	v_cvt_pk_f16_f32 v141, v168, v169
	v_cvt_pk_f16_f32 v140, v166, v167
	s_nop 3
	v_cvt_pk_f16_f32 v136, v156, v157
	v_mfma_f32_16x16x16_f16 v[154:157], v[170:171], v[130:131], 0
	v_cvt_pk_f16_f32 v137, v158, v159
	s_nop 6
	v_cvt_pk_f16_f32 v153, v156, v157
	v_cvt_pk_f16_f32 v152, v154, v155
	s_nop 1
	v_mfma_f32_16x16x16_f16 v[152:155], v[132:133], v[152:153], 0
	s_nop 7
	v_cvt_pk_f16_f32 v132, v152, v153
	v_add_u32_e32 v152, 0x1800, v216
	ds_read_b64_tr_b16 v[156:157], v152
	v_add_u32_e32 v152, 0x1a00, v216
	ds_read_b64_tr_b16 v[158:159], v152
	v_add_u32_e32 v152, 0x1c00, v216
	ds_read_b64_tr_b16 v[162:163], v152
	v_add_u32_e32 v152, 0x1e00, v216
	ds_read_b64_tr_b16 v[164:165], v152
	s_waitcnt lgkmcnt(0)
	v_cvt_pk_f16_f32 v133, v154, v155
	v_cvt_f32_f16_sdwa v161, v156 dst_sel:DWORD dst_unused:UNUSED_PAD src0_sel:WORD_1
	v_cvt_f32_f16_e32 v156, v156
	v_mfma_f32_16x16x16_f16 v[152:155], v[148:149], v[202:203], 0
	v_cvt_f32_f16_e32 v166, v157
	v_cvt_f32_f16_sdwa v157, v157 dst_sel:DWORD dst_unused:UNUSED_PAD src0_sel:WORD_1
	s_nop 5
	v_sub_f32_e32 v152, v156, v152
	v_sub_f32_e32 v153, v161, v153
	v_sub_f32_e32 v154, v166, v154
	v_sub_f32_e32 v155, v157, v155
	v_cvt_pk_f16_f32 v157, v154, v155
	v_cvt_pk_f16_f32 v156, v152, v153
	v_mfma_f32_16x16x16_f16 v[152:155], v[148:149], v[200:201], 0
	v_cvt_f32_f16_e32 v161, v158
	v_cvt_f32_f16_sdwa v158, v158 dst_sel:DWORD dst_unused:UNUSED_PAD src0_sel:WORD_1
	v_cvt_f32_f16_e32 v166, v159
	v_cvt_f32_f16_sdwa v159, v159 dst_sel:DWORD dst_unused:UNUSED_PAD src0_sel:WORD_1
	s_nop 3
	v_sub_f32_e32 v152, v161, v152
	v_sub_f32_e32 v158, v158, v153
	v_sub_f32_e32 v153, v166, v154
	v_sub_f32_e32 v154, v159, v155
	v_cvt_pk_f16_f32 v153, v153, v154
	v_cvt_pk_f16_f32 v152, v152, v158
	ds_write2st64_b64 v160, v[156:157], v[152:153] offset0:8 offset1:9
	v_mfma_f32_16x16x16_f16 v[152:155], v[148:149], v[198:199], 0
	v_cvt_f32_f16_e32 v156, v162
	v_cvt_f32_f16_sdwa v157, v162 dst_sel:DWORD dst_unused:UNUSED_PAD src0_sel:WORD_1
	v_cvt_f32_f16_e32 v158, v163
	v_cvt_f32_f16_sdwa v159, v163 dst_sel:DWORD dst_unused:UNUSED_PAD src0_sel:WORD_1
	v_cvt_f32_f16_e32 v161, v165
	s_nop 2
	v_sub_f32_e32 v152, v156, v152
	v_sub_f32_e32 v153, v157, v153
	v_sub_f32_e32 v154, v158, v154
	v_sub_f32_e32 v155, v159, v155
	v_cvt_pk_f16_f32 v157, v154, v155
	v_cvt_pk_f16_f32 v156, v152, v153
	v_mfma_f32_16x16x16_f16 v[152:155], v[148:149], v[196:197], 0
	v_cvt_f32_f16_e32 v158, v164
	v_cvt_f32_f16_sdwa v159, v164 dst_sel:DWORD dst_unused:UNUSED_PAD src0_sel:WORD_1
	v_cvt_f32_f16_sdwa v162, v165 dst_sel:DWORD dst_unused:UNUSED_PAD src0_sel:WORD_1
	s_nop 4
	v_sub_f32_e32 v152, v158, v152
	v_sub_f32_e32 v158, v159, v153
	v_sub_f32_e32 v153, v161, v154
	v_sub_f32_e32 v154, v162, v155
	v_cvt_pk_f16_f32 v153, v153, v154
	v_cvt_pk_f16_f32 v152, v152, v158
	ds_write2st64_b64 v160, v[156:157], v[152:153] offset0:10 offset1:11
	s_waitcnt lgkmcnt(0)
	v_add_u32_e32 v152, 0x1000, v216
	ds_read_b64_tr_b16 v[152:153], v152
	v_add_u32_e32 v154, 0x1200, v216
	ds_read_b64_tr_b16 v[158:159], v154
	v_add_u32_e32 v154, 0x1400, v216
	ds_read_b64_tr_b16 v[206:207], v154
	v_add_u32_e32 v154, 0x1600, v216
	ds_read_b64_tr_b16 v[204:205], v154
	s_waitcnt lgkmcnt(0)
	v_cvt_pk_f16_f32 v183, v4, v5
	v_cvt_pk_f16_f32 v182, v2, v3
	v_mfma_f32_16x16x16_f16 v[154:157], v[150:151], v[142:143], 0
	v_cvt_pk_f16_f32 v189, v44, v45
	v_cvt_pk_f16_f32 v188, v42, v43
	v_cvt_pk_f16_f32 v187, v8, v9
	v_mfma_f32_16x16x16_f16 v[160:163], v[148:149], v[146:147], 0
	v_cvt_pk_f16_f32 v186, v6, v7
	v_cvt_pk_f16_f32 v193, v68, v69
	v_cvt_pk_f16_f32 v192, v66, v67
	v_mfma_f32_16x16x16_f16 v[2:5], v[152:153], v[182:183], 0
	v_cvt_pk_f16_f32 v191, v12, v13
	s_nop 2
	v_sub_f32_e32 v157, v157, v163
	v_sub_f32_e32 v156, v156, v162
	v_sub_f32_e32 v155, v155, v161
	v_sub_f32_e32 v154, v154, v160
	v_mfma_f32_16x16x16_f16 v[2:5], v[158:159], v[188:189], v[2:5]
	v_cvt_pk_f16_f32 v190, v10, v11
	v_cvt_pk_f16_f32 v81, v80, v81
	v_cvt_pk_f16_f32 v80, v78, v79
	v_mfma_f32_16x16x16_f16 v[6:9], v[152:153], v[186:187], v[154:157]
	v_cvt_pk_f16_f32 v195, v16, v17
	v_cvt_pk_f16_f32 v194, v14, v15
	v_cvt_pk_f16_f32 v41, v40, v41
	v_mfma_f32_16x16x16_f16 v[2:5], v[206:207], v[192:193], v[2:5]
	v_cvt_pk_f16_f32 v40, v38, v39
	v_lshlrev_b32_e32 v10, 1, v144
	v_add3_u32 v38, s36, v10, v178
	v_mfma_f32_16x16x16_f16 v[6:9], v[158:159], v[190:191], v[6:9]
	v_cvt_pk_f16_f32 v167, v92, v93
	v_cvt_pk_f16_f32 v166, v90, v91
	v_cvt_pk_f16_f32 v169, v28, v29
	v_mfma_f32_16x16x16_f16 v[2:5], v[204:205], v[80:81], v[2:5]
	v_cvt_pk_f16_f32 v168, v26, v27
	v_cvt_pk_f16_f32 v173, v76, v77
	v_cvt_pk_f16_f32 v172, v74, v75
	v_mfma_f32_16x16x16_f16 v[6:9], v[206:207], v[194:195], v[6:9]
	v_cvt_pk_f16_f32 v177, v20, v21
	s_nop 2
	v_cvt_f16_f32_e32 v2, v2
	v_cvt_f16_f32_e32 v4, v4
	v_mfma_f32_16x16x16_f16 v[6:9], v[204:205], v[40:41], v[6:9]
	v_cvt_pk_f16_f32 v176, v18, v19
	ds_write_b16 v38, v2
	v_cvt_f16_f32_e32 v2, v3
	v_mfma_f32_16x16x16_f16 v[10:13], v[150:151], v[138:139], 0
	v_cvt_pk_f16_f32 v181, v84, v85
	s_nop 2
	v_cvt_f16_f32_e32 v6, v6
	v_cvt_f16_f32_e32 v3, v7
	v_mfma_f32_16x16x16_f16 v[14:17], v[148:149], v[140:141], 0
	ds_write_b16 v38, v2 offset:128
	v_cvt_f16_f32_e32 v2, v8
	ds_write_b16 v38, v6 offset:6144
	v_mfma_f32_16x16x16_f16 v[42:45], v[152:153], v[166:167], 0
	v_cvt_f16_f32_e32 v6, v5
	s_nop 2
	v_sub_f32_e32 v13, v13, v17
	v_sub_f32_e32 v12, v12, v16
	v_sub_f32_e32 v11, v11, v15
	v_sub_f32_e32 v10, v10, v14
	v_mfma_f32_16x16x16_f16 v[14:17], v[158:159], v[172:173], v[42:45]
	ds_write_b16 v38, v3 offset:6272
	ds_write_b16 v38, v4 offset:256
	ds_write_b16 v38, v2 offset:6400
	v_cvt_pk_f16_f32 v180, v82, v83
	v_mfma_f32_16x16x16_f16 v[10:13], v[152:153], v[168:169], v[10:13]
	ds_write_b16 v38, v6 offset:384
	v_cvt_f16_f32_e32 v6, v9
	v_cvt_pk_f16_f32 v185, v24, v25
	v_mfma_f32_16x16x16_f16 v[2:5], v[158:159], v[176:177], v[10:13]
	v_cvt_pk_f16_f32 v184, v22, v23
	v_cvt_pk_f16_f32 v89, v88, v89
	v_cvt_pk_f16_f32 v88, v86, v87
	v_mfma_f32_16x16x16_f16 v[10:13], v[206:207], v[180:181], v[14:17]
	ds_write_b16 v38, v6 offset:6528
	v_cvt_pk_f16_f32 v33, v32, v33
	v_cvt_pk_f16_f32 v32, v30, v31
	v_mfma_f32_16x16x16_f16 v[2:5], v[206:207], v[184:185], v[2:5]
	v_cvt_pk_f16_f32 v161, v112, v113
	v_cvt_pk_f16_f32 v160, v110, v111
	v_cvt_pk_f16_f32 v163, v60, v61
	v_mfma_f32_16x16x16_f16 v[6:9], v[204:205], v[88:89], v[10:13]
	v_cvt_pk_f16_f32 v162, v58, v59
	v_cvt_pk_f16_f32 v165, v96, v97
	v_cvt_pk_f16_f32 v164, v94, v95
	v_mfma_f32_16x16x16_f16 v[10:13], v[150:151], v[134:135], 0
	v_cvt_pk_f16_f32 v171, v36, v37
	s_nop 2
	v_cvt_f16_f32_e32 v6, v6
	v_cvt_pk_f16_f32 v170, v34, v35
	v_mfma_f32_16x16x16_f16 v[14:17], v[148:149], v[136:137], 0
	v_cvt_pk_f16_f32 v175, v104, v105
	ds_write_b16 v38, v6 offset:32
	v_cvt_f16_f32_e32 v6, v7
	v_mfma_f32_16x16x16_f16 v[2:5], v[204:205], v[32:33], v[2:5]
	v_cvt_pk_f16_f32 v174, v102, v103
	s_nop 2
	v_sub_f32_e32 v13, v13, v17
	v_sub_f32_e32 v12, v12, v16
	v_sub_f32_e32 v11, v11, v15
	v_mfma_f32_16x16x16_f16 v[16:19], v[152:153], v[160:161], 0
	v_sub_f32_e32 v10, v10, v14
	v_cvt_f16_f32_e32 v2, v2
	v_cvt_f16_f32_e32 v3, v3
	v_mfma_f32_16x16x16_f16 v[10:13], v[152:153], v[162:163], v[10:13]
	ds_write_b16 v38, v2 offset:6176
	ds_write_b16 v38, v6 offset:160
	ds_write_b16 v38, v3 offset:6304
	v_cvt_f16_f32_e32 v2, v8
	v_mfma_f32_16x16x16_f16 v[14:17], v[158:159], v[164:165], v[16:19]
	v_cvt_pk_f16_f32 v179, v52, v53
	v_cvt_pk_f16_f32 v178, v50, v51
	ds_write_b16 v38, v2 offset:288
	v_mfma_f32_16x16x16_f16 v[10:13], v[158:159], v[170:171], v[10:13]
	v_cvt_f16_f32_e32 v2, v4
	v_cvt_pk_f16_f32 v109, v108, v109
	v_cvt_pk_f16_f32 v108, v106, v107
	v_mfma_f32_16x16x16_f16 v[14:17], v[206:207], v[174:175], v[14:17]
	v_cvt_f16_f32_e32 v18, v9
	v_cvt_pk_f16_f32 v57, v56, v57
	v_cvt_pk_f16_f32 v56, v54, v55
	v_mfma_f32_16x16x16_f16 v[10:13], v[206:207], v[178:179], v[10:13]
	ds_write_b16 v38, v2 offset:6432
	v_cvt_pk_f16_f32 v157, v116, v117
	v_cvt_pk_f16_f32 v156, v114, v115
	v_mfma_f32_16x16x16_f16 v[6:9], v[204:205], v[108:109], v[14:17]
	v_cvt_pk_f16_f32 v155, v100, v101
	v_cvt_pk_f16_f32 v154, v98, v99
	v_cvt_pk_f16_f32 v125, v124, v125
	v_cvt_f16_f32_e32 v14, v5
	v_mfma_f32_16x16x16_f16 v[2:5], v[204:205], v[56:57], v[10:13]
	s_nop 2
	v_cvt_f16_f32_e32 v6, v6
	v_cvt_pk_f16_f32 v124, v122, v123
	v_cvt_pk_f16_f32 v129, v128, v129
	v_mfma_f32_16x16x16_f16 v[10:13], v[150:151], v[130:131], 0
	v_cvt_pk_f16_f32 v151, v72, v73
	v_cvt_f16_f32_e32 v2, v2
	ds_write_b16 v38, v18 offset:416
	ds_write_b16 v38, v14 offset:6560
	ds_write_b16 v38, v6 offset:64
	ds_write_b16 v38, v2 offset:6208
	v_mfma_f32_16x16x16_f16 v[14:17], v[148:149], v[132:133], 0
	v_cvt_f16_f32_e32 v2, v7
	v_cvt_pk_f16_f32 v149, v64, v65
	v_cvt_pk_f16_f32 v148, v62, v63
	v_cvt_f16_f32_e32 v3, v3
	v_cvt_f16_f32_e32 v6, v8
	s_nop 2
	v_sub_f32_e32 v13, v13, v17
	v_sub_f32_e32 v12, v12, v16
	v_sub_f32_e32 v11, v11, v15
	v_mfma_f32_16x16x16_f16 v[16:19], v[152:153], v[156:157], 0
	v_sub_f32_e32 v10, v10, v14
	ds_write_b16 v38, v2 offset:192
	ds_write_b16 v38, v3 offset:6336
	ds_write_b16 v38, v6 offset:320
	v_cvt_f16_f32_e32 v2, v4
	v_mfma_f32_16x16x16_f16 v[10:13], v[152:153], v[148:149], v[10:13]
	v_cvt_pk_f16_f32 v153, v48, v49
	v_cvt_pk_f16_f32 v152, v46, v47
	ds_write_b16 v38, v2 offset:6464
	v_mfma_f32_16x16x16_f16 v[14:17], v[158:159], v[154:155], v[16:19]
	v_cvt_f16_f32_e32 v2, v9
	v_cvt_pk_f16_f32 v150, v70, v71
	v_cvt_pk_f16_f32 v128, v126, v127
	v_mfma_f32_16x16x16_f16 v[10:13], v[158:159], v[152:153], v[10:13]
	v_cvt_pk_f16_f32 v159, v120, v121
	v_cvt_pk_f16_f32 v158, v118, v119
	ds_write_b16 v38, v2 offset:448
	v_mfma_f32_16x16x16_f16 v[10:13], v[206:207], v[150:151], v[10:13]
	v_mfma_f32_16x16x16_f16 v[6:9], v[206:207], v[158:159], v[14:17]
	s_nop 2
	v_cvt_f16_f32_e32 v14, v5
	v_mfma_f32_16x16x16_f16 v[2:5], v[204:205], v[124:125], v[6:9]
	ds_write_b16 v38, v14 offset:6592
	v_mfma_f32_16x16x16_f16 v[6:9], v[204:205], v[128:129], v[10:13]
	s_nop 5
	v_cvt_f16_f32_e32 v2, v2
	s_nop 0
	v_cvt_f16_f32_e32 v6, v6
	v_cvt_f16_f32_e32 v3, v3
	v_cvt_f16_f32_e32 v7, v7
	ds_write_b16 v38, v2 offset:96
	ds_write_b16 v38, v6 offset:6240
	ds_write_b16 v38, v3 offset:224
	ds_write_b16 v38, v7 offset:6368
	v_cvt_f16_f32_e32 v2, v4
	v_cvt_f16_f32_e32 v3, v8
	v_cvt_f16_f32_e32 v4, v5
	v_cvt_f16_f32_e32 v5, v9
	ds_write_b16 v38, v2 offset:352
	ds_write_b16 v38, v3 offset:6496
	ds_write_b16 v38, v4 offset:480
	ds_write_b16 v38, v5 offset:6624
	v_add_u32_e32 v2, 0x2000, v216
	ds_read_b64_tr_b16 v[62:63], v2
	v_add_u32_e32 v3, 0x2800, v216
	ds_read_b64_tr_b16 v[64:65], v3
	v_add_u32_e32 v2, 0x2200, v216
	ds_read_b64_tr_b16 v[46:47], v2
	v_add_u32_e32 v2, 0x2a00, v216
	ds_read_b64_tr_b16 v[48:49], v2
	v_add_u32_e32 v2, 0x2400, v216
	ds_read_b64_tr_b16 v[118:119], v2
	v_add_u32_e32 v2, 0x2c00, v216
	ds_read_b64_tr_b16 v[120:121], v2
	v_add_u32_e32 v2, 0x2600, v216
	ds_read_b64_tr_b16 v[70:71], v2
	v_add_u32_e32 v2, 0x2e00, v216
	ds_read_b64_tr_b16 v[72:73], v2
	v_add_u32_e32 v2, 0x4000, v215
	ds_read2_b32 v[10:11], v2 offset1:16
	ds_read2_b32 v[18:19], v2 offset0:32 offset1:48
	s_waitcnt lgkmcnt(0)
	v_mfma_f32_16x16x16_f16 v[2:5], v[202:203], v[62:63], 0
	v_cmp_eq_u32_e32 vcc, v208, v144
	v_cmp_eq_u32_e64 s[0:1], v211, v144
	v_cmp_eq_u32_e64 s[2:3], v209, v144
	v_mfma_f32_16x16x16_f16 v[6:9], v[202:203], v[46:47], 0
	s_waitcnt lgkmcnt(1)
	v_cndmask_b32_e32 v12, 0, v10, vcc
	s_nop 1
	v_sub_f32_e32 v2, v12, v2
	v_cndmask_b32_e64 v12, 0, v10, s[0:1]
	v_mfma_f32_16x16x16_f16 v[24:27], v[202:203], v[70:71], 0
	v_cmp_eq_u32_e64 s[4:5], v210, v144
	v_sub_f32_e32 v3, v12, v3
	v_cndmask_b32_e64 v12, 0, v10, s[2:3]
	v_cndmask_b32_e64 v10, 0, v10, s[4:5]
	v_mfma_f32_16x16x16_f16 v[20:23], v[202:203], v[118:119], 0
	v_sub_f32_e32 v5, v10, v5
	v_cvt_pk_f16_f32 v98, v2, v3
	v_cvt_f16_f32_e64 v6, -v6
	v_mfma_f32_16x16x16_f16 v[28:31], v[200:201], v[62:63], 0
	v_mov_b32_e32 v2, v7
	v_cvt_f16_f32_e64 v7, -v9
	v_cvt_f16_f32_e64 v10, -v24
	v_sub_f32_e32 v4, v12, v4
	v_mov_b32_e32 v3, v8
	v_mov_b32_e32 v12, v25
	v_mov_b32_e32 v13, v26
	v_add_f32_e64 v2, -v2, 0
	v_add_f32_e64 v3, -v3, 0
	v_add_f32_e64 v12, -v12, 0
	v_add_f32_e64 v13, -v13, 0
	v_cvt_pk_f16_f32 v8, v2, v3
	v_cvt_pk_f16_f32 v54, v12, v13
	v_cvt_pk_f16_f32 v99, v4, v5
	v_mfma_f32_16x16x16_f16 v[2:5], v[198:199], v[62:63], 0
	v_pack_b32_f16 v100, v6, v8
	v_alignbit_b32 v101, v7, v8, 16
	v_cvt_f16_f32_e64 v8, -v20
	v_cvt_f16_f32_e64 v9, -v23
	v_pack_b32_f16 v122, v10, v54
	v_cvt_f16_f32_e64 v10, -v28
	v_mov_b32_e32 v12, v29
	v_mov_b32_e32 v13, v30
	v_cvt_f16_f32_e64 v38, -v31
	v_mfma_f32_16x16x16_f16 v[28:31], v[64:65], v[142:143], 0
	v_mov_b32_e32 v6, v21
	v_mov_b32_e32 v7, v22
	v_add_f32_e64 v6, -v6, 0
	v_add_f32_e64 v7, -v7, 0
	v_mfma_f32_16x16x16_f16 v[82:85], v[62:63], v[146:147], 0
	v_add_f32_e64 v12, -v12, 0
	v_add_f32_e64 v13, -v13, 0
	v_cvt_pk_f16_f32 v6, v6, v7
	v_cvt_pk_f16_f32 v12, v12, v13
	v_pack_b32_f16 v126, v8, v6
	v_alignbit_b32 v127, v9, v6, 16
	v_mfma_f32_16x16x16_f16 v[6:9], v[196:197], v[62:63], 0
	v_pack_b32_f16 v114, v10, v12
	v_alignbit_b32 v115, v38, v12, 16
	v_cvt_f16_f32_e64 v10, -v2
	v_sub_f32_e32 v31, v31, v85
	v_sub_f32_e32 v30, v30, v84
	v_sub_f32_e32 v29, v29, v83
	v_sub_f32_e32 v28, v28, v82
	v_cvt_f16_f32_e64 v12, -v5
	v_mov_b32_e32 v2, v3
	v_mov_b32_e32 v3, v4
	v_mfma_f32_16x16x16_f16 v[28:31], v[98:99], v[186:187], v[28:31]
	v_add_f32_e64 v2, -v2, 0
	v_add_f32_e64 v3, -v3, 0
	v_cvt_f16_f32_e64 v55, -v27
	v_cvt_pk_f16_f32 v13, v2, v3
	v_pack_b32_f16 v116, v10, v13
	v_alignbit_b32 v117, v12, v13, 16
	v_cvt_f16_f32_e64 v10, -v6
	v_mfma_f32_16x16x16_f16 v[34:37], v[200:201], v[46:47], 0
	v_mov_b32_e32 v6, v7
	v_mov_b32_e32 v7, v8
	v_cvt_f16_f32_e64 v8, -v9
	v_mfma_f32_16x16x16_f16 v[28:31], v[114:115], v[190:191], v[28:31]
	v_add_f32_e64 v6, -v6, 0
	v_add_f32_e64 v7, -v7, 0
	v_alignbit_b32 v123, v55, v54, 16
	v_cvt_pk_f16_f32 v6, v6, v7
	v_mfma_f32_16x16x16_f16 v[42:45], v[198:199], v[46:47], 0
	s_waitcnt lgkmcnt(0)
	v_add_u32_e32 v144, s36, v213
	s_add_u32 s26, s26, 16
	v_mfma_f32_16x16x16_f16 v[58:61], v[198:199], v[118:119], 0
	s_addc_u32 s27, s27, 0
	s_nop 3
	v_cvt_f16_f32_e64 v42, -v42
	s_cmpk_eq_i32 s26, 0x100
	v_mfma_f32_16x16x16_f16 v[20:23], v[198:199], v[70:71], 0
	v_pack_b32_f16 v198, v10, v6
	v_cndmask_b32_e32 v10, 0, v11, vcc
	v_alignbit_b32 v199, v8, v6, 16
	v_mfma_f32_16x16x16_f16 v[6:9], v[116:117], v[194:195], v[28:31]
	s_nop 2
	v_sub_f32_e32 v28, v10, v34
	v_cndmask_b32_e64 v10, 0, v11, s[0:1]
	v_sub_f32_e32 v29, v10, v35
	v_cndmask_b32_e64 v10, 0, v11, s[2:3]
	v_cndmask_b32_e64 v11, 0, v11, s[4:5]
	v_sub_f32_e32 v10, v10, v36
	v_sub_f32_e32 v11, v11, v37
	v_mfma_f32_16x16x16_f16 v[66:69], v[196:197], v[46:47], 0
	v_mov_b32_e32 v34, v43
	v_mov_b32_e32 v35, v44
	v_add_f32_e64 v38, -v34, 0
	v_add_f32_e64 v39, -v35, 0
	v_mfma_f32_16x16x16_f16 v[24:27], v[196:197], v[118:119], 0
	v_cvt_f16_f32_e64 v43, -v45
	v_cvt_pk_f16_f32 v38, v38, v39
	v_pack_b32_f16 v202, v42, v38
	v_mfma_f32_16x16x16_f16 v[74:77], v[196:197], v[70:71], 0
	v_cvt_pk_f16_f32 v197, v10, v11
	v_cvt_pk_f16_f32 v196, v28, v29
	v_alignbit_b32 v203, v43, v38, 16
	v_mfma_f32_16x16x16_f16 v[10:13], v[48:49], v[142:143], 0
	v_mfma_f32_16x16x16_f16 v[28:31], v[46:47], v[146:147], 0
	v_mfma_f32_16x16x16_f16 v[34:37], v[100:101], v[182:183], 0
	v_mfma_f32_16x16x16_f16 v[50:53], v[200:201], v[118:119], 0
	s_nop 5
	v_sub_f32_e32 v13, v13, v31
	v_sub_f32_e32 v12, v12, v30
	v_sub_f32_e32 v11, v11, v29
	v_sub_f32_e32 v10, v10, v28
	v_mfma_f32_16x16x16_f16 v[28:31], v[196:197], v[188:189], v[34:37]
	s_nop 2
	v_cvt_f16_f32_e64 v36, -v66
	v_cvt_f16_f32_e64 v37, -v69
	v_mov_b32_e32 v34, v67
	v_mov_b32_e32 v35, v68
	v_add_f32_e64 v34, -v34, 0
	v_add_f32_e64 v35, -v35, 0
	v_mfma_f32_16x16x16_f16 v[28:31], v[202:203], v[192:193], v[28:31]
	v_cvt_pk_f16_f32 v34, v34, v35
	v_pack_b32_f16 v210, v36, v34
	v_alignbit_b32 v211, v37, v34, 16
	v_cvt_f16_f32_e64 v36, -v50
	v_mov_b32_e32 v34, v51
	v_mfma_f32_16x16x16_f16 v[42:45], v[210:211], v[80:81], v[28:31]
	v_mov_b32_e32 v35, v52
	s_nop 1
	v_cvt_f16_f32_e64 v30, -v53
	v_add_f32_e64 v28, -v34, 0
	v_add_f32_e64 v29, -v35, 0
	s_waitcnt lgkmcnt(0)
	v_cndmask_b32_e32 v34, 0, v18, vcc
	v_cvt_pk_f16_f32 v28, v28, v29
	v_pack_b32_f16 v206, v36, v28
	v_alignbit_b32 v207, v30, v28, 16
	v_sub_f32_e32 v38, v34, v58
	v_cndmask_b32_e64 v34, 0, v18, s[0:1]
	v_cndmask_b32_e64 v50, 0, v18, s[2:3]
	v_mfma_f32_16x16x16_f16 v[28:31], v[120:121], v[142:143], 0
	v_sub_f32_e32 v39, v34, v59
	v_sub_f32_e32 v58, v50, v60
	v_cndmask_b32_e64 v18, 0, v18, s[4:5]
	v_mfma_f32_16x16x16_f16 v[34:37], v[118:119], v[146:147], 0
	v_sub_f32_e32 v18, v18, v61
	v_cvt_pk_f16_f32 v205, v58, v18
	v_cvt_pk_f16_f32 v204, v38, v39
	v_mfma_f32_16x16x16_f16 v[50:53], v[126:127], v[182:183], 0
	v_cvt_f16_f32_e64 v18, -v24
	s_nop 2
	v_sub_f32_e32 v31, v31, v37
	v_sub_f32_e32 v30, v30, v36
	v_sub_f32_e32 v29, v29, v35
	v_sub_f32_e32 v28, v28, v34
	v_mfma_f32_16x16x16_f16 v[34:37], v[206:207], v[188:189], v[50:53]
	v_mov_b32_e32 v24, v25
	v_mov_b32_e32 v25, v26
	v_add_f32_e64 v38, -v24, 0
	v_add_f32_e64 v39, -v25, 0
	v_cvt_f16_f32_e64 v50, -v27
	v_mfma_f32_16x16x16_f16 v[28:31], v[126:127], v[186:187], v[28:31]
	v_mfma_f32_16x16x16_f16 v[24:27], v[204:205], v[192:193], v[34:37]
	s_nop 2
	v_cvt_pk_f16_f32 v34, v38, v39
	v_pack_b32_f16 v208, v18, v34
	v_alignbit_b32 v209, v50, v34, 16
	v_mfma_f32_16x16x16_f16 v[14:17], v[200:201], v[70:71], 0
	v_cvt_f16_f32_e64 v50, -v23
	v_mfma_f32_16x16x16_f16 v[28:31], v[206:207], v[190:191], v[28:31]
	v_mfma_f32_16x16x16_f16 v[28:31], v[204:205], v[194:195], v[28:31]
	s_nop 4
	v_cvt_f16_f32_e64 v18, -v14
	v_mov_b32_e32 v14, v15
	v_mov_b32_e32 v15, v16
	v_mfma_f32_16x16x16_f16 v[66:69], v[208:209], v[80:81], v[24:27]
	s_nop 2
	v_cvt_f16_f32_e64 v26, -v17
	v_add_f32_e64 v24, -v14, 0
	v_add_f32_e64 v25, -v15, 0
	v_mfma_f32_16x16x16_f16 v[14:17], v[208:209], v[40:41], v[28:31]
	v_cvt_pk_f16_f32 v24, v24, v25
	v_pack_b32_f16 v200, v18, v24
	v_alignbit_b32 v201, v26, v24, 16
	v_mfma_f32_16x16x16_f16 v[24:27], v[72:73], v[142:143], 0
	v_cvt_f16_f32_e64 v18, -v20
	v_mov_b32_e32 v20, v21
	v_mov_b32_e32 v21, v22
	v_mfma_f32_16x16x16_f16 v[28:31], v[70:71], v[146:147], 0
	v_add_f32_e64 v38, -v20, 0
	v_add_f32_e64 v39, -v21, 0
	v_mfma_f32_16x16x16_f16 v[90:93], v[98:99], v[182:183], 0
	v_mfma_f32_16x16x16_f16 v[10:13], v[100:101], v[186:187], v[10:13]
	s_nop 3
	v_sub_f32_e32 v23, v27, v31
	v_sub_f32_e32 v22, v26, v30
	v_sub_f32_e32 v21, v25, v29
	v_sub_f32_e32 v20, v24, v28
	v_mfma_f32_16x16x16_f16 v[34:37], v[122:123], v[182:183], 0
	v_cvt_pk_f16_f32 v24, v38, v39
	v_pack_b32_f16 v146, v18, v24
	v_alignbit_b32 v147, v50, v24, 16
	v_mfma_f32_16x16x16_f16 v[20:23], v[122:123], v[186:187], v[20:23]
	v_cndmask_b32_e32 v18, 0, v19, vcc
	v_sub_f32_e32 v28, v18, v74
	v_cndmask_b32_e64 v18, 0, v19, s[0:1]
	v_mfma_f32_16x16x16_f16 v[2:5], v[114:115], v[188:189], v[90:93]
	v_sub_f32_e32 v29, v18, v75
	v_cndmask_b32_e64 v18, 0, v19, s[2:3]
	v_cndmask_b32_e64 v19, 0, v19, s[4:5]
	v_mfma_f32_16x16x16_f16 v[10:13], v[196:197], v[190:191], v[10:13]
	v_sub_f32_e32 v18, v18, v76
	v_sub_f32_e32 v19, v19, v77
	v_cvt_pk_f16_f32 v143, v18, v19
	v_mfma_f32_16x16x16_f16 v[24:27], v[200:201], v[188:189], v[34:37]
	v_cvt_pk_f16_f32 v142, v28, v29
	v_mfma_f32_16x16x16_f16 v[20:23], v[200:201], v[190:191], v[20:23]
	v_mfma_f32_16x16x16_f16 v[2:5], v[116:117], v[192:193], v[2:5]
	v_mfma_f32_16x16x16_f16 v[10:13], v[202:203], v[194:195], v[10:13]
	v_mfma_f32_16x16x16_f16 v[24:27], v[146:147], v[192:193], v[24:27]
	v_mfma_f32_16x16x16_f16 v[18:21], v[146:147], v[194:195], v[20:23]
	v_mfma_f32_16x16x16_f16 v[2:5], v[198:199], v[80:81], v[2:5]
	v_mfma_f32_16x16x16_f16 v[6:9], v[198:199], v[40:41], v[6:9]
	v_mfma_f32_16x16x16_f16 v[10:13], v[210:211], v[40:41], v[10:13]
	v_mfma_f32_16x16x16_f16 v[78:81], v[142:143], v[80:81], v[24:27]
	v_mfma_f32_16x16x16_f16 v[38:41], v[142:143], v[40:41], v[18:21]
	v_mfma_f32_16x16x16_f16 v[18:21], v[64:65], v[138:139], 0
	v_mfma_f32_16x16x16_f16 v[22:25], v[62:63], v[140:141], 0
	v_mfma_f32_16x16x16_f16 v[26:29], v[98:99], v[166:167], 0
	v_mfma_f32_16x16x16_f16 v[34:37], v[100:101], v[166:167], 0
	s_nop 5
	v_sub_f32_e32 v21, v21, v25
	v_sub_f32_e32 v20, v20, v24
	v_sub_f32_e32 v19, v19, v23
	v_sub_f32_e32 v18, v18, v22
	v_mfma_f32_16x16x16_f16 v[22:25], v[114:115], v[172:173], v[26:29]
	s_nop 0
	v_mfma_f32_16x16x16_f16 v[18:21], v[98:99], v[168:169], v[18:21]
	v_mfma_f32_16x16x16_f16 v[18:21], v[114:115], v[176:177], v[18:21]
	v_mfma_f32_16x16x16_f16 v[22:25], v[116:117], v[180:181], v[22:25]
	v_mfma_f32_16x16x16_f16 v[18:21], v[116:117], v[184:185], v[18:21]
	v_mfma_f32_16x16x16_f16 v[90:93], v[198:199], v[88:89], v[22:25]
	v_mfma_f32_16x16x16_f16 v[26:29], v[198:199], v[32:33], v[18:21]
	v_mfma_f32_16x16x16_f16 v[18:21], v[48:49], v[138:139], 0
	v_mfma_f32_16x16x16_f16 v[22:25], v[46:47], v[140:141], 0
	v_mfma_f32_16x16x16_f16 v[50:53], v[126:127], v[166:167], 0
	v_mfma_f32_16x16x16_f16 v[58:61], v[122:123], v[166:167], 0
	s_nop 5
	v_sub_f32_e32 v21, v21, v25
	v_sub_f32_e32 v20, v20, v24
	v_sub_f32_e32 v19, v19, v23
	v_sub_f32_e32 v18, v18, v22
	v_mfma_f32_16x16x16_f16 v[22:25], v[196:197], v[172:173], v[34:37]
	v_mfma_f32_16x16x16_f16 v[22:25], v[202:203], v[180:181], v[22:25]
	v_mfma_f32_16x16x16_f16 v[74:77], v[210:211], v[88:89], v[22:25]
	v_mfma_f32_16x16x16_f16 v[22:25], v[120:121], v[138:139], 0
	v_mfma_f32_16x16x16_f16 v[34:37], v[118:119], v[140:141], 0
	v_mfma_f32_16x16x16_f16 v[18:21], v[100:101], v[168:169], v[18:21]
	v_mfma_f32_16x16x16_f16 v[18:21], v[196:197], v[176:177], v[18:21]
	s_nop 5
	v_sub_f32_e32 v25, v25, v37
	v_sub_f32_e32 v24, v24, v36
	v_sub_f32_e32 v23, v23, v35
	v_sub_f32_e32 v22, v22, v34
	v_mfma_f32_16x16x16_f16 v[34:37], v[206:207], v[172:173], v[50:53]
	v_mfma_f32_16x16x16_f16 v[34:37], v[204:205], v[180:181], v[34:37]
	v_mfma_f32_16x16x16_f16 v[82:85], v[208:209], v[88:89], v[34:37]
	v_mfma_f32_16x16x16_f16 v[34:37], v[72:73], v[138:139], 0
	v_mfma_f32_16x16x16_f16 v[50:53], v[70:71], v[140:141], 0
	v_mfma_f32_16x16x16_f16 v[22:25], v[126:127], v[168:169], v[22:25]
	v_mfma_f32_16x16x16_f16 v[22:25], v[206:207], v[176:177], v[22:25]
	s_nop 5
	v_sub_f32_e32 v37, v37, v53
	v_sub_f32_e32 v36, v36, v52
	v_sub_f32_e32 v35, v35, v51
	v_sub_f32_e32 v34, v34, v50
	v_mfma_f32_16x16x16_f16 v[50:53], v[200:201], v[172:173], v[58:61]
	s_nop 0
	v_mfma_f32_16x16x16_f16 v[34:37], v[122:123], v[168:169], v[34:37]
	v_mfma_f32_16x16x16_f16 v[34:37], v[200:201], v[176:177], v[34:37]
	v_mfma_f32_16x16x16_f16 v[18:21], v[202:203], v[184:185], v[18:21]
	v_mfma_f32_16x16x16_f16 v[22:25], v[204:205], v[184:185], v[22:25]
	v_mfma_f32_16x16x16_f16 v[50:53], v[146:147], v[180:181], v[50:53]
	v_mfma_f32_16x16x16_f16 v[34:37], v[146:147], v[184:185], v[34:37]
	v_mfma_f32_16x16x16_f16 v[18:21], v[210:211], v[32:33], v[18:21]
	v_mfma_f32_16x16x16_f16 v[22:25], v[208:209], v[32:33], v[22:25]
	v_mfma_f32_16x16x16_f16 v[86:89], v[142:143], v[88:89], v[50:53]
	v_mfma_f32_16x16x16_f16 v[30:33], v[142:143], v[32:33], v[34:37]
	v_mfma_f32_16x16x16_f16 v[34:37], v[64:65], v[134:135], 0
	v_mfma_f32_16x16x16_f16 v[50:53], v[62:63], v[136:137], 0
	v_mfma_f32_16x16x16_f16 v[58:61], v[98:99], v[160:161], 0
	v_mfma_f32_16x16x16_f16 v[94:97], v[100:101], v[160:161], 0
	s_nop 5
	v_sub_f32_e32 v37, v37, v53
	v_sub_f32_e32 v36, v36, v52
	v_sub_f32_e32 v35, v35, v51
	v_sub_f32_e32 v34, v34, v50
	v_mfma_f32_16x16x16_f16 v[50:53], v[114:115], v[164:165], v[58:61]
	s_nop 0
	v_mfma_f32_16x16x16_f16 v[34:37], v[98:99], v[162:163], v[34:37]
	v_mfma_f32_16x16x16_f16 v[34:37], v[114:115], v[170:171], v[34:37]
	v_mfma_f32_16x16x16_f16 v[50:53], v[116:117], v[174:175], v[50:53]
	v_mfma_f32_16x16x16_f16 v[34:37], v[116:117], v[178:179], v[34:37]
	v_mfma_f32_16x16x16_f16 v[110:113], v[198:199], v[108:109], v[50:53]
	v_mfma_f32_16x16x16_f16 v[58:61], v[198:199], v[56:57], v[34:37]
	v_mfma_f32_16x16x16_f16 v[34:37], v[48:49], v[134:135], 0
	v_mfma_f32_16x16x16_f16 v[50:53], v[46:47], v[136:137], 0
	v_mfma_f32_16x16x16_f16 v[102:105], v[118:119], v[136:137], 0
	v_mfma_f32_16x16x16_f16 v[138:141], v[126:127], v[160:161], 0
	s_nop 5
	v_sub_f32_e32 v37, v37, v53
	v_sub_f32_e32 v36, v36, v52
	v_sub_f32_e32 v35, v35, v51
	v_sub_f32_e32 v34, v34, v50
	v_mfma_f32_16x16x16_f16 v[50:53], v[196:197], v[164:165], v[94:97]
	v_mfma_f32_16x16x16_f16 v[50:53], v[202:203], v[174:175], v[50:53]
	v_mfma_f32_16x16x16_f16 v[94:97], v[210:211], v[108:109], v[50:53]
	v_mfma_f32_16x16x16_f16 v[50:53], v[120:121], v[134:135], 0
	v_mfma_f32_16x16x16_f16 v[34:37], v[100:101], v[162:163], v[34:37]
	v_mfma_f32_16x16x16_f16 v[166:169], v[122:123], v[160:161], 0
	s_nop 5
	v_sub_f32_e32 v53, v53, v105
	v_sub_f32_e32 v52, v52, v104
	v_sub_f32_e32 v51, v51, v103
	v_sub_f32_e32 v50, v50, v102
	v_mfma_f32_16x16x16_f16 v[102:105], v[206:207], v[164:165], v[138:141]
	v_mfma_f32_16x16x16_f16 v[138:141], v[72:73], v[134:135], 0
	v_mfma_f32_16x16x16_f16 v[134:137], v[70:71], v[136:137], 0
	v_mfma_f32_16x16x16_f16 v[50:53], v[126:127], v[162:163], v[50:53]
	v_mfma_f32_16x16x16_f16 v[34:37], v[196:197], v[170:171], v[34:37]
	s_nop 5
	v_sub_f32_e32 v137, v141, v137
	v_sub_f32_e32 v136, v140, v136
	v_sub_f32_e32 v135, v139, v135
	v_sub_f32_e32 v134, v138, v134
	v_mfma_f32_16x16x16_f16 v[50:53], v[206:207], v[170:171], v[50:53]
	s_nop 0
	v_mfma_f32_16x16x16_f16 v[134:137], v[122:123], v[162:163], v[134:137]
	ds_read_b128 v[160:163], v144 offset:6144
	v_mfma_f32_16x16x16_f16 v[134:137], v[200:201], v[170:171], v[134:137]
	v_mfma_f32_16x16x16_f16 v[138:141], v[200:201], v[164:165], v[166:169]
	v_mfma_f32_16x16x16_f16 v[34:37], v[202:203], v[178:179], v[34:37]
	v_mfma_f32_16x16x16_f16 v[50:53], v[204:205], v[178:179], v[50:53]
	v_mfma_f32_16x16x16_f16 v[134:137], v[146:147], v[178:179], v[134:137]
	v_mfma_f32_16x16x16_f16 v[102:105], v[204:205], v[174:175], v[102:105]
	v_mfma_f32_16x16x16_f16 v[138:141], v[146:147], v[174:175], v[138:141]
	v_mfma_f32_16x16x16_f16 v[34:37], v[210:211], v[56:57], v[34:37]
	v_mfma_f32_16x16x16_f16 v[50:53], v[208:209], v[56:57], v[50:53]
	v_mfma_f32_16x16x16_f16 v[54:57], v[142:143], v[56:57], v[134:137]
	v_mfma_f32_16x16x16_f16 v[134:137], v[64:65], v[130:131], 0
	v_mfma_f32_16x16x16_f16 v[62:65], v[62:63], v[132:133], 0
	v_mfma_f32_16x16x16_f16 v[102:105], v[208:209], v[108:109], v[102:105]
	v_mfma_f32_16x16x16_f16 v[106:109], v[142:143], v[108:109], v[138:141]
	s_nop 5
	v_sub_f32_e32 v65, v137, v65
	v_sub_f32_e32 v64, v136, v64
	v_sub_f32_e32 v63, v135, v63
	v_mfma_f32_16x16x16_f16 v[138:141], v[98:99], v[156:157], 0
	v_sub_f32_e32 v62, v134, v62
	s_nop 1
	v_mfma_f32_16x16x16_f16 v[62:65], v[98:99], v[148:149], v[62:65]
	v_mfma_f32_16x16x16_f16 v[134:137], v[114:115], v[154:155], v[138:141]
	v_mfma_f32_16x16x16_f16 v[62:65], v[114:115], v[152:153], v[62:65]
	v_mfma_f32_16x16x16_f16 v[134:137], v[116:117], v[158:159], v[134:137]
	v_mfma_f32_16x16x16_f16 v[62:65], v[116:117], v[150:151], v[62:65]
	v_mfma_f32_16x16x16_f16 v[114:117], v[198:199], v[124:125], v[134:137]
	v_mfma_f32_16x16x16_f16 v[134:137], v[48:49], v[130:131], 0
	v_mfma_f32_16x16x16_f16 v[46:49], v[46:47], v[132:133], 0
	v_mfma_f32_16x16x16_f16 v[138:141], v[100:101], v[156:157], 0
	v_mfma_f32_16x16x16_f16 v[62:65], v[198:199], v[128:129], v[62:65]
	s_nop 5
	v_sub_f32_e32 v49, v137, v49
	v_sub_f32_e32 v48, v136, v48
	v_sub_f32_e32 v47, v135, v47
	v_sub_f32_e32 v46, v134, v46
	v_mfma_f32_16x16x16_f16 v[134:137], v[120:121], v[130:131], 0
	v_mfma_f32_16x16x16_f16 v[118:121], v[118:119], v[132:133], 0
	v_mfma_f32_16x16x16_f16 v[46:49], v[100:101], v[148:149], v[46:49]
	v_mfma_f32_16x16x16_f16 v[98:101], v[196:197], v[154:155], v[138:141]
	s_nop 5
	v_sub_f32_e32 v121, v137, v121
	v_sub_f32_e32 v120, v136, v120
	v_sub_f32_e32 v119, v135, v119
	v_mfma_f32_16x16x16_f16 v[138:141], v[126:127], v[156:157], 0
	v_sub_f32_e32 v118, v134, v118
	s_nop 1
	v_mfma_f32_16x16x16_f16 v[118:121], v[126:127], v[148:149], v[118:121]
	v_ashrrev_i32_e32 v126, 3, v212
	v_ashrrev_i32_e32 v127, 31, v126
	v_lshl_add_u64 v[126:127], s[28:29], 0, v[126:127]
	v_mfma_f32_16x16x16_f16 v[134:137], v[206:207], v[154:155], v[138:141]
	v_lshlrev_b64 v[126:127], 11, v[126:127]
	v_mfma_f32_16x16x16_f16 v[118:121], v[206:207], v[152:153], v[118:121]
	v_mfma_f32_16x16x16_f16 v[138:141], v[72:73], v[130:131], 0
	v_mfma_f32_16x16x16_f16 v[70:73], v[70:71], v[132:133], 0
	v_mfma_f32_16x16x16_f16 v[134:137], v[204:205], v[158:159], v[134:137]
	v_mfma_f32_16x16x16_f16 v[46:49], v[196:197], v[152:153], v[46:49]
	s_nop 5
	v_sub_f32_e32 v133, v141, v73
	v_sub_f32_e32 v132, v140, v72
	v_sub_f32_e32 v131, v139, v71
	v_sub_f32_e32 v130, v138, v70
	v_mfma_f32_16x16x16_f16 v[70:73], v[204:205], v[150:151], v[118:121]
	v_and_or_b32 v138, v214, 56, s6
	v_lshlrev_b32_e32 v164, 1, v138
	v_or_b32_e32 v126, v126, v164
	v_mfma_f32_16x16x16_f16 v[118:121], v[208:209], v[124:125], v[134:137]
	s_nop 2
	ds_read_b128 v[134:137], v144
	v_mfma_f32_16x16x16_f16 v[138:141], v[122:123], v[156:157], 0
	v_lshl_add_u64 v[156:157], s[10:11], 0, v[126:127]
	s_waitcnt lgkmcnt(0)
	global_store_dwordx4 v[156:157], v[134:137], off
	v_mfma_f32_16x16x16_f16 v[130:133], v[122:123], v[148:149], v[130:133]
	v_lshl_add_u64 v[122:123], s[12:13], 0, v[126:127]
	v_add_u32_e32 v126, 64, v212
	global_store_dwordx4 v[122:123], v[160:163], off
	v_mfma_f32_16x16x16_f16 v[134:137], v[200:201], v[154:155], v[138:141]
	v_ashrrev_i32_e32 v122, 3, v126
	v_lshl_add_u32 v126, v126, 4, s36
	v_ashrrev_i32_e32 v123, 31, v122
	v_mfma_f32_16x16x16_f16 v[130:133], v[200:201], v[152:153], v[130:133]
	ds_read_b128 v[138:141], v126
	ds_read_b128 v[152:155], v126 offset:6144
	v_lshl_add_u64 v[122:123], s[28:29], 0, v[122:123]
	v_mfma_f32_16x16x16_f16 v[98:101], v[202:203], v[158:159], v[98:101]
	v_lshlrev_b64 v[122:123], 11, v[122:123]
	v_or_b32_e32 v122, v122, v164
	v_lshl_add_u64 v[126:127], s[10:11], 0, v[122:123]
	v_mfma_f32_16x16x16_f16 v[46:49], v[202:203], v[150:151], v[46:49]
	v_lshl_add_u64 v[122:123], s[12:13], 0, v[122:123]
	s_waitcnt lgkmcnt(1)
	global_store_dwordx4 v[126:127], v[138:141], off
	s_waitcnt lgkmcnt(0)
	global_store_dwordx4 v[122:123], v[152:155], off
	v_mfma_f32_16x16x16_f16 v[134:137], v[146:147], v[158:159], v[134:137]
	s_waitcnt lgkmcnt(0)
	v_mfma_f32_16x16x16_f16 v[130:133], v[146:147], v[150:151], v[130:133]
	v_mfma_f32_16x16x16_f16 v[98:101], v[210:211], v[124:125], v[98:101]
	v_mfma_f32_16x16x16_f16 v[46:49], v[210:211], v[128:129], v[46:49]
	v_mfma_f32_16x16x16_f16 v[70:73], v[208:209], v[128:129], v[70:73]
	v_mfma_f32_16x16x16_f16 v[122:125], v[142:143], v[124:125], v[134:137]
	v_mfma_f32_16x16x16_f16 v[126:129], v[142:143], v[128:129], v[130:133]
	s_cbranch_scc1 .LBB0_1287

.LBB0_1306:
	s_or_b64 exec, exec, s[0:1]
	v_add_f32_e32 v137, v153, v137
	v_sub_f32_e32 v136, v137, v136
	v_mul_f32_e32 v153, 0x3fb8aa3b, v137
	v_mul_f32_e32 v136, 0x3fb8aa3b, v136
	v_exp_f32_e32 v154, v153
	v_mul_f32_e32 v153, 0xbfb8aa3b, v137
	v_exp_f32_e32 v162, v136
	v_sub_f32_e32 v136, v152, v137
	v_add_f32_e32 v188, v157, v156
	v_add_f32_e32 v156, v135, v134
	v_exp_f32_e32 v159, v153
	v_mul_f32_e32 v136, 0x3fb8aa3b, v136
	v_mul_f32_e32 v134, 0x3fb8aa3b, v156
	v_lshl_add_u64 v[152:153], s[16:17], 0, v[142:143]
	v_exp_f32_e32 v160, v136
	v_exp_f32_e32 v157, v134
	global_load_dwordx4 v[134:137], v[152:153], off
	v_sub_f32_e32 v150, v156, v150
	v_mul_f32_e32 v150, 0x3fb8aa3b, v150
	v_add_f32_e32 v139, v141, v139
	v_exp_f32_e32 v171, v150
	v_sub_f32_e32 v150, v151, v156
	v_sub_f32_e32 v138, v139, v138
	v_mul_f32_e32 v150, 0x3fb8aa3b, v150
	v_mul_f32_e32 v141, 0x3fb8aa3b, v139
	v_mul_f32_e32 v138, 0x3fb8aa3b, v138
	v_mul_f32_e32 v158, 0xbfb8aa3b, v156
	v_exp_f32_e32 v165, v150
	v_exp_f32_e32 v156, v141
	v_mul_f32_e32 v141, 0xbfb8aa3b, v139
	v_exp_f32_e32 v170, v138
	v_sub_f32_e32 v138, v140, v139
	v_lshl_add_u64 v[150:151], s[18:19], 0, v[142:143]
	v_exp_f32_e32 v167, v141
	v_mul_f32_e32 v164, 0x3fb8aa3b, v138
	global_load_dwordx4 v[138:141], v[150:151], off
	v_add_f32_e32 v182, v169, v166
	v_sub_f32_e32 v131, v182, v131
	v_mul_f32_e32 v131, 0x3fb8aa3b, v131
	v_exp_f32_e32 v191, v131
	v_sub_f32_e32 v131, v175, v182
	v_mul_f32_e32 v131, 0x3fb8aa3b, v131
	v_exp_f32_e32 v175, v131
	v_add_f32_e32 v131, v177, v168
	v_mul_f32_e32 v168, 0x3fb8aa3b, v131
	v_mul_f32_e32 v177, 0xbfb8aa3b, v131
	v_sub_f32_e32 v174, v131, v174
	v_sub_f32_e32 v131, v176, v131
	v_mul_f32_e32 v174, 0x3fb8aa3b, v174
	v_mul_f32_e32 v131, 0x3fb8aa3b, v131
	v_exp_f32_e32 v190, v174
	v_exp_f32_e32 v174, v131
	v_add_f32_e32 v131, v173, v148
	v_mul_f32_e32 v148, 0x3fb8aa3b, v131
	v_sub_f32_e32 v130, v131, v130
	v_exp_f32_e32 v173, v148
	v_mul_f32_e32 v148, 0xbfb8aa3b, v131
	v_mul_f32_e32 v130, 0x3fb8aa3b, v130
	v_mul_f32_e32 v166, 0x3fb8aa3b, v182
	v_exp_f32_e32 v176, v148
	v_exp_f32_e32 v187, v130
	v_sub_f32_e32 v130, v149, v131
	v_lshl_add_u64 v[148:149], s[20:21], 0, v[142:143]
	v_exp_f32_e32 v169, v166
	v_mul_f32_e32 v166, 0xbfb8aa3b, v182
	global_load_dwordx4 v[182:185], v[148:149], off
	v_mul_f32_e32 v130, 0x3fb8aa3b, v130
	v_exp_f32_e32 v195, v130
	v_add_f32_e32 v130, v172, v161
	v_mul_f32_e32 v131, 0x3fb8aa3b, v130
	v_exp_f32_e32 v172, v131
	v_mul_f32_e32 v131, 0xbfb8aa3b, v130
	v_exp_f32_e32 v196, v131
	v_sub_f32_e32 v131, v130, v155
	v_sub_f32_e32 v130, v163, v130
	v_mul_f32_e32 v130, 0x3fb8aa3b, v130
	v_exp_f32_e32 v194, v130
	v_mul_f32_e32 v130, 0x3fb8aa3b, v188
	v_exp_f32_e32 v155, v130
	v_mul_f32_e32 v130, 0xbfb8aa3b, v188
	v_exp_f32_e32 v198, v130
	v_sub_f32_e32 v130, v188, v132
	v_mul_f32_e32 v130, 0x3fb8aa3b, v130
	v_mul_f32_e32 v131, 0x3fb8aa3b, v131
	v_exp_f32_e32 v163, v130
	v_sub_f32_e32 v130, v133, v188
	v_exp_f32_e32 v186, v131
	v_mul_f32_e32 v161, 0x3fb8aa3b, v130
	global_load_dwordx4 v[130:133], v[146:147], off offset:16
	v_lshl_add_u64 v[142:143], s[22:23], 0, v[142:143]
	v_or_b32_e32 v197, v180, v178
	v_exp_f32_e32 v177, v177
	v_exp_f32_e32 v166, v166
	v_exp_f32_e32 v164, v164
	v_exp_f32_e32 v158, v158
	v_exp_f32_e32 v161, v161
	s_waitcnt vmcnt(3)
	v_cvt_f32_f16_e32 v146, v134
	v_cvt_f32_f16_sdwa v147, v134 dst_sel:DWORD dst_unused:UNUSED_PAD src0_sel:WORD_1
	v_cvt_f32_f16_e32 v192, v135
	v_cvt_f32_f16_sdwa v193, v135 dst_sel:DWORD dst_unused:UNUSED_PAD src0_sel:WORD_1
	v_exp_f32_e32 v168, v168
	v_mul_f32_e32 v134, v186, v146
	v_mul_f32_e32 v135, v187, v147
	global_load_dwordx4 v[186:189], v[142:143], off
	v_mul_f32_e32 v146, v190, v192
	v_mul_f32_e32 v147, v191, v193
	v_cvt_f32_f16_e32 v190, v136
	v_cvt_f32_f16_sdwa v191, v136 dst_sel:DWORD dst_unused:UNUSED_PAD src0_sel:WORD_1
	v_cvt_f32_f16_e32 v192, v137
	v_cvt_f32_f16_sdwa v193, v137 dst_sel:DWORD dst_unused:UNUSED_PAD src0_sel:WORD_1
	v_cvt_pk_f16_f32 v134, v134, v135
	v_cvt_pk_f16_f32 v135, v146, v147
	v_mul_f32_e32 v136, v170, v190
	v_mul_f32_e32 v137, v171, v191
	v_mul_f32_e32 v146, v162, v192
	v_mul_f32_e32 v147, v163, v193
	v_cvt_pk_f16_f32 v136, v136, v137
	v_cvt_pk_f16_f32 v137, v146, v147
	v_add_u32_e32 v147, s36, v197
	ds_write_b128 v147, v[134:137]
	s_waitcnt vmcnt(3)
	v_cvt_f32_f16_e32 v136, v138
	v_cvt_f32_f16_sdwa v137, v138 dst_sel:DWORD dst_unused:UNUSED_PAD src0_sel:WORD_1
	v_cvt_f32_f16_e32 v162, v139
	v_cvt_f32_f16_sdwa v163, v139 dst_sel:DWORD dst_unused:UNUSED_PAD src0_sel:WORD_1
	v_fma_mixlo_f16 v146, v196, v138, 0 op_sel_hi:[0,1,0]
	v_cvt_f32_f16_e32 v138, v140
	v_cvt_f32_f16_sdwa v139, v140 dst_sel:DWORD dst_unused:UNUSED_PAD src0_sel:WORD_1
	v_mul_f32_e32 v134, v194, v136
	v_mul_f32_e32 v135, v195, v137
	v_pk_mov_b32 v[136:137], v[136:137], v[162:163] op_sel:[1,0]
	v_cvt_pk_f16_f32 v134, v134, v135
	v_mul_f32_e32 v136, v176, v136
	v_mul_f32_e32 v137, v177, v137
	s_nop 0
	v_cvt_pk_f16_f32 v170, v136, v137
	v_mul_f32_e32 v136, v174, v162
	v_mul_f32_e32 v137, v175, v163
	v_pack_b32_f16 v190, v146, v170
	v_cvt_pk_f16_f32 v135, v136, v137
	v_pk_mov_b32 v[136:137], v[162:163], v[138:139] op_sel:[1,0]
	v_cvt_f32_f16_e32 v162, v141
	v_cvt_f32_f16_sdwa v163, v141 dst_sel:DWORD dst_unused:UNUSED_PAD src0_sel:WORD_1
	v_mul_f32_e32 v136, v166, v136
	v_mul_f32_e32 v137, v167, v137
	s_nop 0
	v_cvt_pk_f16_f32 v140, v136, v137
	v_mul_f32_e32 v136, v164, v138
	v_mul_f32_e32 v137, v165, v139
	v_pk_mov_b32 v[138:139], v[138:139], v[162:163] op_sel:[1,0]
	v_cvt_pk_f16_f32 v136, v136, v137
	v_mul_f32_e32 v138, v158, v138
	v_mul_f32_e32 v139, v159, v139
	v_alignbit_b32 v191, v140, v170, 16
	v_cvt_pk_f16_f32 v137, v138, v139
	v_lshrrev_b32_e32 v193, 16, v137
	v_mul_f32_e32 v138, v160, v162
	v_mul_f32_e32 v139, v161, v163
	v_alignbit_b32 v192, v137, v140, 16
	v_cvt_pk_f16_f32 v137, v138, v139
	v_fma_mixhi_f16 v193, v198, v141, 0 op_sel:[0,1,0] op_sel_hi:[0,1,0]
	ds_write_b128 v147, v[190:193] offset:2048
	ds_write_b128 v147, v[134:137] offset:8192
	s_waitcnt vmcnt(2)
	v_cvt_f32_f16_e32 v136, v182
	v_cvt_f32_f16_sdwa v137, v182 dst_sel:DWORD dst_unused:UNUSED_PAD src0_sel:WORD_1
	v_cvt_f32_f16_e32 v140, v183
	v_cvt_f32_f16_sdwa v141, v183 dst_sel:DWORD dst_unused:UNUSED_PAD src0_sel:WORD_1
	v_cvt_f32_f16_e32 v162, v184
	v_cvt_f32_f16_sdwa v163, v184 dst_sel:DWORD dst_unused:UNUSED_PAD src0_sel:WORD_1
	v_mul_f32_e32 v134, v194, v136
	v_mul_f32_e32 v135, v195, v137
	v_pk_mov_b32 v[136:137], v[136:137], v[140:141] op_sel:[1,0]
	v_cvt_pk_f16_f32 v134, v134, v135
	v_mul_f32_e32 v136, v176, v136
	v_mul_f32_e32 v137, v177, v137
	v_fma_mixlo_f16 v138, v196, v182, 0 op_sel_hi:[0,1,0]
	v_cvt_pk_f16_f32 v139, v136, v137
	v_mul_f32_e32 v136, v174, v140
	v_mul_f32_e32 v137, v175, v141
	v_pack_b32_f16 v138, v138, v139
	v_cvt_pk_f16_f32 v135, v136, v137
	v_pk_mov_b32 v[136:137], v[140:141], v[162:163] op_sel:[1,0]
	s_nop 0
	v_mul_f32_e32 v136, v166, v136
	v_mul_f32_e32 v137, v167, v137
	v_cvt_f32_f16_e32 v166, v185
	v_cvt_f32_f16_sdwa v167, v185 dst_sel:DWORD dst_unused:UNUSED_PAD src0_sel:WORD_1
	v_cvt_pk_f16_f32 v146, v136, v137
	v_mul_f32_e32 v136, v164, v162
	v_mul_f32_e32 v137, v165, v163
	v_alignbit_b32 v139, v146, v139, 16
	v_pk_mov_b32 v[140:141], v[162:163], v[166:167] op_sel:[1,0]
	v_cvt_pk_f16_f32 v136, v136, v137
	v_mul_f32_e32 v140, v158, v140
	v_mul_f32_e32 v141, v159, v141
	v_mul_f32_e32 v158, v160, v166
	v_mul_f32_e32 v159, v161, v167
	v_cvt_pk_f16_f32 v137, v140, v141
	v_lshrrev_b32_e32 v141, 16, v137
	v_alignbit_b32 v140, v137, v146, 16
	v_fma_mixhi_f16 v141, v198, v185, 0 op_sel:[0,1,0] op_sel_hi:[0,1,0]
	ds_write_b128 v147, v[138:141] offset:4096
	s_waitcnt vmcnt(0)
	v_cvt_f32_f16_e32 v138, v186
	v_cvt_f32_f16_sdwa v139, v186 dst_sel:DWORD dst_unused:UNUSED_PAD src0_sel:WORD_1
	v_cvt_pk_f16_f32 v137, v158, v159
	v_cvt_f32_f16_e32 v140, v187
	v_cvt_f32_f16_sdwa v141, v187 dst_sel:DWORD dst_unused:UNUSED_PAD src0_sel:WORD_1
	ds_write_b128 v147, v[134:137] offset:10240
	v_cvt_f32_f16_e32 v136, v188
	v_cvt_f32_f16_sdwa v137, v188 dst_sel:DWORD dst_unused:UNUSED_PAD src0_sel:WORD_1
	v_mul_f32_e32 v134, v172, v138
	v_mul_f32_e32 v135, v173, v139
	v_mul_f32_e32 v136, v156, v136
	v_mul_f32_e32 v137, v157, v137
	v_cvt_pk_f16_f32 v138, v134, v135
	v_mul_f32_e32 v134, v168, v140
	v_mul_f32_e32 v135, v169, v141
	v_cvt_pk_f16_f32 v140, v136, v137
	v_cvt_pk_f16_f32 v139, v134, v135
	v_cvt_f32_f16_e32 v134, v189
	v_cvt_f32_f16_sdwa v135, v189 dst_sel:DWORD dst_unused:UNUSED_PAD src0_sel:WORD_1
	v_cvt_f32_f16_e32 v137, v130
	v_mul_f32_e32 v134, v154, v134
	v_mul_f32_e32 v135, v155, v135
	s_nop 0
	v_cvt_pk_f16_f32 v141, v134, v135
	v_add_f32_dpp v134, v137, v137 row_shr:1 row_mask:0xf bank_mask:0xf bound_ctrl:1
	ds_write_b128 v147, v[138:141] offset:6144
	v_mov_b32_e32 v154, 0
	v_add_f32_dpp v134, v134, v134 row_shr:2 row_mask:0xf bank_mask:0xf bound_ctrl:1
	s_nop 1
	v_add_f32_dpp v139, v134, v134 row_shr:4 row_mask:0xf bank_mask:0xf bound_ctrl:1
	v_add_f32_dpp v134, v137, v137 quad_perm:[1,0,3,2] row_mask:0xf bank_mask:0xf bound_ctrl:1
	s_nop 0
	v_mov_b32_dpp v154, v139 row_shr:8 row_mask:0xf bank_mask:0xf
	v_add_f32_dpp v134, v134, v134 quad_perm:[2,3,0,1] row_mask:0xf bank_mask:0xf bound_ctrl:1
	s_nop 1
	v_add_f32_dpp v134, v134, v134 row_half_mirror row_mask:0xf bank_mask:0xf bound_ctrl:1
	s_nop 1
	v_add_f32_dpp v155, v134, v134 row_mirror row_mask:0xf bank_mask:0xf bound_ctrl:1
	s_and_saveexec_b64 s[0:1], vcc
	s_cbranch_execz .LBB0_1308
	v_mul_f32_e32 v134, 0x3fb8aa3b, v155
	v_exp_f32_e32 v134, v134
	ds_write_b32 v181, v134 offset:16416

.LBB0_1322:
	s_or_b64 exec, exec, s[0:1]
	v_add_f32_e32 v174, v174, v130
	v_mul_f32_e32 v130, 0x3fb8aa3b, v174
	v_mul_f32_e32 v133, 0xbfb8aa3b, v174
	v_sub_f32_e32 v136, v174, v136
	v_sub_f32_e32 v138, v138, v174
	global_load_dwordx4 v[174:177], v[152:153], off offset:16
	v_add_f32_e32 v152, v135, v132
	v_sub_f32_e32 v141, v152, v141
	v_mul_f32_e32 v132, 0x3fb8aa3b, v152
	v_mul_f32_e32 v141, 0x3fb8aa3b, v141
	v_add_f32_e32 v181, v173, v172
	v_exp_f32_e32 v135, v132
	v_mul_f32_e32 v132, 0xbfb8aa3b, v152
	v_exp_f32_e32 v183, v141
	v_sub_f32_e32 v141, v171, v152
	v_add_f32_e32 v152, v170, v134
	global_load_dwordx4 v[170:173], v[150:151], off offset:16
	v_add_f32_e32 v150, v167, v165
	v_sub_f32_e32 v131, v150, v131
	v_mul_f32_e32 v131, 0x3fb8aa3b, v131
	v_exp_f32_e32 v167, v131
	v_sub_f32_e32 v131, v166, v150
	v_sub_f32_e32 v140, v152, v140
	v_mul_f32_e32 v131, 0x3fb8aa3b, v131
	v_mul_f32_e32 v140, 0x3fb8aa3b, v140
	v_exp_f32_e32 v185, v131
	v_add_f32_e32 v131, v163, v161
	v_mul_f32_e32 v134, 0x3fb8aa3b, v152
	v_mul_f32_e32 v153, 0xbfb8aa3b, v152
	v_exp_f32_e32 v182, v140
	v_sub_f32_e32 v140, v169, v152
	v_mul_f32_e32 v151, 0x3fb8aa3b, v150
	v_mul_f32_e32 v152, 0xbfb8aa3b, v150
	v_mul_f32_e32 v150, 0x3fb8aa3b, v131
	v_mul_f32_e32 v161, 0xbfb8aa3b, v131
	v_sub_f32_e32 v160, v131, v160
	v_sub_f32_e32 v131, v162, v131
	v_mul_f32_e32 v131, 0x3fb8aa3b, v131
	v_exp_f32_e32 v184, v131
	v_add_f32_e32 v131, v159, v158
	v_mul_f32_e32 v160, 0x3fb8aa3b, v160
	v_mul_f32_e32 v158, 0x3fb8aa3b, v131
	v_exp_f32_e32 v187, v161
	v_exp_f32_e32 v166, v160
	v_exp_f32_e32 v189, v158
	global_load_dwordx4 v[158:161], v[148:149], off offset:16
	v_mul_f32_e32 v162, 0xbfb8aa3b, v131
	v_sub_f32_e32 v148, v131, v156
	v_sub_f32_e32 v131, v157, v131
	v_mul_f32_e32 v131, 0x3fb8aa3b, v131
	v_exp_f32_e32 v191, v131
	v_add_f32_e32 v131, v139, v154
	v_mul_f32_e32 v139, 0x3fb8aa3b, v131
	v_exp_f32_e32 v188, v139
	v_mul_f32_e32 v139, 0xbfb8aa3b, v131
	v_sub_f32_e32 v137, v131, v137
	v_sub_f32_e32 v131, v155, v131
	global_load_dwordx4 v[154:157], v[142:143], off offset:16
	v_mul_f32_e32 v148, 0x3fb8aa3b, v148
	v_mul_f32_e32 v137, 0x3fb8aa3b, v137
	v_exp_f32_e32 v186, v162
	v_exp_f32_e32 v149, v148
	v_exp_f32_e32 v148, v137
	v_mul_f32_e32 v137, 0xbfb8aa3b, v181
	v_exp_f32_e32 v193, v137
	v_sub_f32_e32 v137, v181, v164
	v_mul_f32_e32 v136, 0x3fb8aa3b, v136
	v_mul_f32_e32 v137, 0x3fb8aa3b, v137
	v_exp_f32_e32 v136, v136
	v_exp_f32_e32 v137, v137
	v_mul_f32_e32 v131, 0x3fb8aa3b, v131
	v_exp_f32_e32 v190, v131
	v_exp_f32_e32 v153, v153
	v_exp_f32_e32 v152, v152
	v_mul_f32_e32 v141, 0x3fb8aa3b, v141
	v_mul_f32_e32 v140, 0x3fb8aa3b, v140
	v_exp_f32_e32 v192, v139
	v_exp_f32_e32 v141, v141
	v_exp_f32_e32 v140, v140
	v_exp_f32_e32 v133, v133
	v_exp_f32_e32 v132, v132
	v_sub_f32_e32 v139, v168, v181
	v_mul_f32_e32 v138, 0x3fb8aa3b, v138
	v_mul_f32_e32 v139, 0x3fb8aa3b, v139
	v_exp_f32_e32 v138, v138
	s_waitcnt vmcnt(3)
	v_cvt_f32_f16_sdwa v163, v174 dst_sel:DWORD dst_unused:UNUSED_PAD src0_sel:WORD_1
	v_cvt_f32_f16_e32 v162, v174
	v_cvt_f32_f16_sdwa v165, v175 dst_sel:DWORD dst_unused:UNUSED_PAD src0_sel:WORD_1
	v_cvt_f32_f16_e32 v164, v175
	v_exp_f32_e32 v139, v139
	v_mul_f32_e32 v142, v148, v162
	v_mul_f32_e32 v143, v149, v163
	v_cvt_f32_f16_sdwa v149, v176 dst_sel:DWORD dst_unused:UNUSED_PAD src0_sel:WORD_1
	v_cvt_pk_f16_f32 v162, v142, v143
	v_mul_f32_e32 v142, v166, v164
	v_mul_f32_e32 v143, v167, v165
	v_cvt_f32_f16_e32 v148, v176
	v_cvt_f32_f16_sdwa v167, v177 dst_sel:DWORD dst_unused:UNUSED_PAD src0_sel:WORD_1
	v_cvt_f32_f16_e32 v166, v177
	v_cvt_pk_f16_f32 v163, v142, v143
	v_mul_f32_e32 v142, v182, v148
	v_mul_f32_e32 v143, v183, v149
	v_mul_f32_e32 v131, 0x3fb8aa3b, v181
	v_mul_f32_e32 v136, v136, v166
	v_mul_f32_e32 v137, v137, v167
	v_cvt_pk_f16_f32 v164, v142, v143
	v_cvt_pk_f16_f32 v165, v136, v137
	s_waitcnt vmcnt(2)
	v_cvt_f32_f16_sdwa v137, v170 dst_sel:DWORD dst_unused:UNUSED_PAD src0_sel:WORD_1
	v_cvt_f32_f16_e32 v136, v170
	v_cvt_f32_f16_sdwa v143, v171 dst_sel:DWORD dst_unused:UNUSED_PAD src0_sel:WORD_1
	v_cvt_f32_f16_e32 v142, v171
	ds_write_b128 v147, v[162:165] offset:16
	v_mul_f32_e32 v148, v190, v136
	v_mul_f32_e32 v149, v191, v137
	v_fma_mixlo_f16 v163, v192, v170, 0 op_sel_hi:[0,1,0]
	v_pk_mov_b32 v[136:137], v[136:137], v[142:143] op_sel:[1,0]
	v_cvt_pk_f16_f32 v162, v148, v149
	v_mul_f32_e32 v136, v186, v136
	v_mul_f32_e32 v137, v187, v137
	v_mul_f32_e32 v148, v184, v142
	v_mul_f32_e32 v149, v185, v143
	v_cvt_pk_f16_f32 v164, v136, v137
	v_cvt_f32_f16_sdwa v137, v172 dst_sel:DWORD dst_unused:UNUSED_PAD src0_sel:WORD_1
	v_cvt_f32_f16_e32 v136, v172
	v_pack_b32_f16 v166, v163, v164
	v_cvt_pk_f16_f32 v163, v148, v149
	v_exp_f32_e32 v130, v130
	v_pk_mov_b32 v[142:143], v[142:143], v[136:137] op_sel:[1,0]
	v_mul_f32_e32 v148, v140, v136
	v_mul_f32_e32 v149, v141, v137
	v_mul_f32_e32 v142, v152, v142
	v_mul_f32_e32 v143, v153, v143
	v_exp_f32_e32 v134, v134
	v_cvt_pk_f16_f32 v165, v142, v143
	v_cvt_f32_f16_sdwa v143, v173 dst_sel:DWORD dst_unused:UNUSED_PAD src0_sel:WORD_1
	v_cvt_f32_f16_e32 v142, v173
	v_alignbit_b32 v167, v165, v164, 16
	v_cvt_pk_f16_f32 v164, v148, v149
	v_exp_f32_e32 v151, v151
	v_pk_mov_b32 v[136:137], v[136:137], v[142:143] op_sel:[1,0]
	v_exp_f32_e32 v150, v150
	v_mul_f32_e32 v136, v132, v136
	v_mul_f32_e32 v137, v133, v137
	v_exp_f32_e32 v131, v131
	v_cvt_pk_f16_f32 v136, v136, v137
	v_alignbit_b32 v168, v136, v165, 16
	v_lshrrev_b32_e32 v169, 16, v136
	v_mul_f32_e32 v136, v138, v142
	v_mul_f32_e32 v137, v139, v143
	s_waitcnt vmcnt(1)
	v_cvt_f32_f16_sdwa v143, v159 dst_sel:DWORD dst_unused:UNUSED_PAD src0_sel:WORD_1
	v_cvt_pk_f16_f32 v165, v136, v137
	v_cvt_f32_f16_sdwa v137, v158 dst_sel:DWORD dst_unused:UNUSED_PAD src0_sel:WORD_1
	v_cvt_f32_f16_e32 v136, v158
	v_cvt_f32_f16_e32 v142, v159
	v_fma_mixhi_f16 v169, v193, v173, 0 op_sel:[0,1,0] op_sel_hi:[0,1,0]
	ds_write_b128 v147, v[166:169] offset:2064
	ds_write_b128 v147, v[162:165] offset:8208
	v_mul_f32_e32 v148, v190, v136
	v_mul_f32_e32 v149, v191, v137
	v_pk_mov_b32 v[136:137], v[136:137], v[142:143] op_sel:[1,0]
	v_cvt_pk_f16_f32 v162, v148, v149
	v_mul_f32_e32 v136, v186, v136
	v_mul_f32_e32 v137, v187, v137
	v_mul_f32_e32 v148, v184, v142
	v_mul_f32_e32 v149, v185, v143
	v_cvt_pk_f16_f32 v159, v136, v137
	v_cvt_f32_f16_sdwa v137, v160 dst_sel:DWORD dst_unused:UNUSED_PAD src0_sel:WORD_1
	v_cvt_f32_f16_e32 v136, v160
	v_cvt_pk_f16_f32 v163, v148, v149
	v_fma_mixlo_f16 v158, v192, v158, 0 op_sel_hi:[0,1,0]
	v_lshlrev_b32_e32 v213, 4, v212
	v_pk_mov_b32 v[142:143], v[142:143], v[136:137] op_sel:[1,0]
	v_mul_f32_e32 v140, v140, v136
	v_mul_f32_e32 v141, v141, v137
	v_mul_f32_e32 v142, v152, v142
	v_mul_f32_e32 v143, v153, v143
	v_cvt_pk_f16_f32 v164, v140, v141
	v_cvt_pk_f16_f32 v148, v142, v143
	v_cvt_f32_f16_sdwa v143, v161 dst_sel:DWORD dst_unused:UNUSED_PAD src0_sel:WORD_1
	v_cvt_f32_f16_e32 v142, v161
	s_waitcnt vmcnt(0)
	v_cvt_f32_f16_sdwa v141, v157 dst_sel:DWORD dst_unused:UNUSED_PAD src0_sel:WORD_1
	v_cvt_f32_f16_e32 v140, v157
	v_pack_b32_f16 v166, v158, v159
	v_pk_mov_b32 v[136:137], v[136:137], v[142:143] op_sel:[1,0]
	v_alignbit_b32 v167, v148, v159, 16
	v_mul_f32_e32 v132, v132, v136
	v_mul_f32_e32 v133, v133, v137
	v_cvt_f32_f16_sdwa v137, v155 dst_sel:DWORD dst_unused:UNUSED_PAD src0_sel:WORD_1
	v_cvt_pk_f16_f32 v132, v132, v133
	v_alignbit_b32 v168, v132, v148, 16
	v_lshrrev_b32_e32 v169, 16, v132
	v_mul_f32_e32 v132, v138, v142
	v_mul_f32_e32 v133, v139, v143
	v_cvt_f32_f16_e32 v136, v155
	v_cvt_pk_f16_f32 v165, v132, v133
	v_cvt_f32_f16_sdwa v133, v154 dst_sel:DWORD dst_unused:UNUSED_PAD src0_sel:WORD_1
	v_cvt_f32_f16_e32 v132, v154
	v_cvt_f32_f16_sdwa v139, v156 dst_sel:DWORD dst_unused:UNUSED_PAD src0_sel:WORD_1
	v_cvt_f32_f16_e32 v138, v156
	v_mul_f32_e32 v136, v150, v136
	v_mul_f32_e32 v137, v151, v137
	v_mul_f32_e32 v132, v188, v132
	v_mul_f32_e32 v133, v189, v133
	v_mul_f32_e32 v130, v130, v140
	v_mul_f32_e32 v131, v131, v141
	v_mul_f32_e32 v134, v134, v138
	v_mul_f32_e32 v135, v135, v139
	v_fma_mixhi_f16 v169, v193, v161, 0 op_sel:[0,1,0] op_sel_hi:[0,1,0]
	v_cvt_pk_f16_f32 v132, v132, v133
	v_cvt_pk_f16_f32 v133, v136, v137
	v_cvt_pk_f16_f32 v134, v134, v135
	v_cvt_pk_f16_f32 v135, v130, v131
	v_and_b32_e32 v130, 0xfffffe00, v213
	v_and_b32_e32 v131, 16, v212
	ds_write_b128 v147, v[166:169] offset:4112
	ds_write_b128 v147, v[162:165] offset:10256
	ds_write_b128 v147, v[132:135] offset:6160
	v_or3_b32 v130, v130, v131, v180
	s_waitcnt lgkmcnt(0)
	v_add_u32_e32 v142, s36, v130
	ds_read_b128 v[130:133], v142
	ds_read_b128 v[134:137], v142 offset:2048
	ds_read_b128 v[138:141], v142 offset:1024
	ds_read_b128 v[148:151], v142 offset:3072
	ds_read_b128 v[156:159], v142 offset:4096
	ds_read_b128 v[160:163], v142 offset:5120
	ds_read_b128 v[164:167], v142 offset:6144
	ds_read_b128 v[168:171], v142 offset:7168
	s_waitcnt lgkmcnt(6)
	v_mfma_f32_16x16x32_f16 v[152:155], v[130:133], v[134:137], 0
	v_lshlrev_b32_e32 v208, 2, v179
	v_lshl_add_u32 v215, v144, 2, s36
	v_cmp_gt_i32_e32 vcc, v208, v144
	s_waitcnt lgkmcnt(3)
	v_mfma_f32_16x16x32_f16 v[130:133], v[130:133], v[156:159], 0
	v_lshl_add_u32 v143, v179, 8, v215
	v_or_b32_e32 v211, 1, v208
	v_or_b32_e32 v209, 2, v208
	s_waitcnt lgkmcnt(1)
	v_mfma_f32_16x16x32_f16 v[134:137], v[164:167], v[134:137], 0
	v_or_b32_e32 v210, 3, v208
	v_mfma_f32_16x16x32_f16 v[156:159], v[164:167], v[156:159], 0
	v_mfma_f32_16x16x32_f16 v[130:133], v[138:141], v[160:163], v[130:133]
	v_mfma_f32_16x16x32_f16 v[152:155], v[138:141], v[148:151], v[152:155]
	s_waitcnt lgkmcnt(0)
	v_mfma_f32_16x16x32_f16 v[134:137], v[168:171], v[148:151], v[134:137]
	s_nop 4
	v_cvt_f16_f32_e32 v130, v130
	v_cvt_f16_f32_e32 v131, v131
	v_cndmask_b32_e32 v142, 0, v152, vcc
	v_mfma_f32_16x16x32_f16 v[138:141], v[168:171], v[160:163], v[156:159]
	v_cndmask_b32_e32 v130, 0, v130, vcc
	v_cvt_f16_f32_e32 v134, v134
	v_cvt_f16_f32_e32 v135, v135
	v_cmp_lt_i32_e32 vcc, v208, v144
	ds_write_b32 v143, v142 offset:14336
	s_nop 2
	v_cvt_f16_f32_e32 v138, v138
	v_cvt_f16_f32_e32 v139, v139
	v_cndmask_b32_e64 v142, v153, 0, vcc
	v_lshl_add_u32 v143, v211, 6, v215
	v_cndmask_b32_e64 v134, v134, 0, vcc
	v_cndmask_b32_e64 v138, v138, 0, vcc
	ds_write_b32 v143, v142 offset:14336
	v_cndmask_b32_e64 v142, v131, 0, vcc
	v_cmp_lt_i32_e32 vcc, v211, v144
	v_lshl_add_u32 v143, v209, 6, v215
	v_cvt_f16_f32_e32 v132, v132
	v_cndmask_b32_e64 v135, v135, 0, vcc
	v_cndmask_b32_e64 v139, v139, 0, vcc
	v_cmp_gt_i32_e32 vcc, v209, v144
	v_add_u32_e32 v161, s36, v180
	v_pack_b32_f16 v130, v130, v142
	v_cndmask_b32_e32 v131, 0, v154, vcc
	ds_write_b32 v143, v131 offset:14336
	v_cvt_f16_f32_e32 v131, v136
	v_cvt_f16_f32_e32 v136, v140
	v_cndmask_b32_e32 v132, 0, v132, vcc
	v_cmp_lt_i32_e32 vcc, v209, v144
	v_lshl_add_u32 v143, v210, 6, v215
	s_nop 0
	v_cndmask_b32_e64 v140, v131, 0, vcc
	v_cvt_f16_f32_e32 v131, v133
	v_cndmask_b32_e64 v136, v136, 0, vcc
	v_cmp_gt_i32_e32 vcc, v210, v144
	s_nop 1
	v_cndmask_b32_e32 v131, 0, v131, vcc
	v_pack_b32_f16 v131, v132, v131
	v_cvt_f16_f32_e32 v132, v137
	v_cvt_f16_f32_e32 v137, v141
	v_cndmask_b32_e32 v133, 0, v155, vcc
	v_cmp_lt_i32_e32 vcc, v210, v144
	ds_write_b32 v143, v133 offset:14336
	s_nop 0
	v_cndmask_b32_e64 v132, v132, 0, vcc
	v_pack_b32_f16 v133, v140, v132
	v_pack_b32_f16 v132, v134, v135
	v_cndmask_b32_e64 v134, v137, 0, vcc
	v_pack_b32_f16 v135, v136, v134
	v_lshlrev_b32_e32 v136, 3, v179
	v_add_u32_e32 v160, v161, v136
	v_pack_b32_f16 v134, v138, v139
	ds_write_b64 v160, v[130:131] offset:15872
	ds_write2st64_b64 v160, v[132:133], v[134:135] offset0:4 offset1:5
	s_waitcnt lgkmcnt(0)
	v_cmp_gt_u32_e32 vcc, 16, v212
	s_and_saveexec_b64 s[0:1], vcc
	s_cbranch_execz .LBB0_1289
	v_mov_b32_e32 v179, s36
	v_add_u32_e32 v214, 0x3800, v179
	ds_read2_b64 v[150:153], v214 offset0:8 offset1:16
	ds_read_b128 v[130:133], v179 offset:14528
	ds_read_b128 v[154:157], v179 offset:14592
	v_cmp_eq_u32_e32 vcc, 0, v144
	s_waitcnt lgkmcnt(2)
	v_mov_b32_e32 v136, v152
	v_cndmask_b32_e64 v148, 0, 1.0, vcc
	v_cmp_eq_u32_e32 vcc, 3, v144
	v_mov_b32_e32 v137, v150
	s_waitcnt lgkmcnt(1)
	v_mov_b32_e32 v158, v131
	v_cndmask_b32_e64 v133, 0, 1.0, vcc
	v_cmp_eq_u32_e32 vcc, 1, v144
	v_fma_f32 v147, -v148, v130, v133
	v_mov_b32_e32 v159, v132
	v_cndmask_b32_e64 v135, 0, 1.0, vcc
	v_cmp_eq_u32_e32 vcc, 2, v144
	s_waitcnt lgkmcnt(0)
	v_mov_b32_e32 v175, v154
	v_mov_b32_e32 v205, v156
	v_cndmask_b32_e64 v134, 0, 1.0, vcc
	v_fma_f32 v150, -v148, v136, v134
	v_fma_f32 v151, -v148, v137, v135
	ds_read_b128 v[140:143], v179 offset:15296
	ds_read_b128 v[136:139], v179 offset:15312
	ds_read_b128 v[162:165], v179 offset:14656
	ds_read_b128 v[130:133], v179 offset:14720
	ds_read_b128 v[166:169], v179 offset:14784
	ds_read_b128 v[170:173], v179 offset:14800
	v_cmp_eq_u32_e32 vcc, 4, v144
	s_waitcnt lgkmcnt(3)
	v_mov_b32_e32 v207, v164
	s_waitcnt lgkmcnt(2)
	v_mov_b32_e32 v206, v132
	v_cndmask_b32_e64 v135, 0, 1.0, vcc
	v_cmp_eq_u32_e32 vcc, 7, v144
	s_waitcnt lgkmcnt(1)
	v_mov_b32_e32 v174, v166
	v_mov_b32_e32 v154, v167
	v_cndmask_b32_e64 v134, 0, 1.0, vcc
	v_fma_f32 v134, -v148, v174, v134
	v_fma_f32 v135, -v148, v175, v135
	v_mov_b32_e32 v204, v168
	v_mov_b32_e32 v156, v169
	v_cmp_eq_u32_e32 vcc, 5, v144
	ds_read2_b64 v[166:169], v214 offset0:42 offset1:50
	v_fma_f32 v176, -v151, v154, v134
	v_fma_f32 v177, -v151, v155, v135
	v_cndmask_b32_e64 v135, 0, 1.0, vcc
	v_cmp_eq_u32_e32 vcc, 6, v144
	v_mov_b32_e32 v154, v130
	v_mov_b32_e32 v155, v162
	v_mov_b32_e32 v162, v131
	v_mov_b32_e32 v164, v133
	s_waitcnt lgkmcnt(0)
	v_mov_b32_e32 v167, v172
	ds_read_b128 v[172:175], v179 offset:14848
	ds_read_b128 v[180:183], v179 offset:14864
	ds_read_b128 v[130:133], v179 offset:14944
	ds_read_b128 v[184:187], v179 offset:14976
	ds_read_b128 v[188:191], v179 offset:14912
	ds_read_b128 v[192:195], v179 offset:14928
	v_cndmask_b32_e64 v134, 0, 1.0, vcc
	v_fma_f32 v134, -v148, v154, v134
	v_fma_f32 v135, -v148, v155, v135
	v_cmp_eq_u32_e32 vcc, 10, v144
	v_mov_b32_e32 v149, v151
	ds_read_b128 v[196:199], v179 offset:14992
	ds_read_b128 v[200:203], v179 offset:15040
	s_waitcnt lgkmcnt(5)
	v_cndmask_b32_e64 v131, 0, 1.0, vcc
	s_waitcnt lgkmcnt(4)
	v_mul_f32_e32 v132, v148, v184
	v_mul_f32_e32 v133, v149, v185
	v_fma_f32 v162, -v151, v162, v134
	v_fma_f32 v163, -v151, v163, v135
	v_sub_f32_e32 v131, v131, v132
	v_sub_f32_e32 v131, v131, v133
	ds_read2_b64 v[132:135], v214 offset0:84 offset1:110
	v_cmp_eq_u32_e32 vcc, 11, v144
	v_mov_b32_e32 v152, v151
	s_waitcnt lgkmcnt(1)
	v_mov_b32_e32 v184, v201
	s_waitcnt lgkmcnt(0)
	v_cndmask_b32_e64 v135, 0, 1.0, vcc
	v_fma_f32 v154, -v148, v200, v135
	v_mov_b32_e32 v185, v151
	v_mov_b32_e32 v155, v150
	v_fma_f32 v152, -v152, v184, v154
	v_fma_f32 v153, -v153, v185, v155
	v_mov_b32_e32 v154, v151
	v_mov_b32_e32 v155, v153
	v_mul_f32_e32 v154, v158, v154
	v_mul_f32_e32 v155, v159, v155
	v_fma_f32 v158, -v153, v204, v176
	v_fma_f32 v159, -v153, v205, v177
	v_sub_f32_e32 v135, v147, v154
	v_sub_f32_e32 v154, v135, v155
	v_fma_f32 v156, -v154, v156, v158
	v_fma_f32 v157, -v154, v157, v159
	v_fma_f32 v158, -v153, v206, v162
	v_fma_f32 v159, -v153, v207, v163
	v_mov_b32_e32 v162, v153
	v_mov_b32_e32 v163, v154
	v_mov_b32_e32 v216, v168
	v_mov_b32_e32 v217, v166
	v_fma_f32 v158, -v154, v164, v158
	v_fma_f32 v159, -v154, v165, v159
	v_mul_f32_e32 v162, v162, v186
	v_mul_f32_e32 v163, v163, v187
	v_fma_f32 v158, -v216, v157, v158
	v_fma_f32 v159, -v217, v157, v159
	v_sub_f32_e32 v131, v131, v162
	v_sub_f32_e32 v131, v131, v163
	v_mov_b32_e32 v162, v157
	v_mov_b32_e32 v163, v159
	v_mul_f32_e32 v162, v162, v196
	v_mul_f32_e32 v163, v163, v197
	v_mov_b32_e32 v166, v171
	v_sub_f32_e32 v131, v131, v162
	v_sub_f32_e32 v131, v131, v163
	ds_read_b128 v[162:165], v179 offset:15056
	ds_read_b128 v[184:187], v179 offset:15072
	v_fma_f32 v135, -v157, v170, v156
	v_mov_b32_e32 v155, v157
	v_mov_b32_e32 v170, v203
	s_waitcnt lgkmcnt(1)
	v_mov_b32_e32 v171, v162
	v_fma_f32 v147, -v153, v202, v152
	v_mul_f32_e32 v170, v154, v170
	v_mul_f32_e32 v171, v155, v171
	v_mov_b32_e32 v168, v159
	v_sub_f32_e32 v147, v147, v170
	v_sub_f32_e32 v162, v147, v171
	v_mov_b32_e32 v170, v163
	v_mov_b32_e32 v171, v159
	v_mov_b32_e32 v163, v158
	v_fma_f32 v196, -v168, v170, v162
	v_fma_f32 v197, -v169, v171, v163
	v_mov_b32_e32 v162, v159
	v_mov_b32_e32 v163, v197
	v_mul_f32_e32 v162, v166, v162
	v_mul_f32_e32 v163, v167, v163
	v_mov_b32_e32 v200, v197
	v_sub_f32_e32 v135, v135, v162
	v_sub_f32_e32 v201, v135, v163
	v_mul_f32_e32 v162, v200, v198
	v_mul_f32_e32 v163, v201, v199
	v_cmp_eq_u32_e32 vcc, 8, v144
	v_sub_f32_e32 v131, v131, v162
	v_sub_f32_e32 v131, v131, v163
	v_cndmask_b32_e64 v163, 0, 1.0, vcc
	v_cmp_eq_u32_e32 vcc, 9, v144
	v_mov_b32_e32 v166, v188
	v_mov_b32_e32 v167, v172
	v_cndmask_b32_e64 v162, 0, 1.0, vcc
	v_fma_f32 v162, -v148, v166, v162
	v_fma_f32 v163, -v148, v167, v163
	v_mov_b32_e32 v172, v189
	v_fma_f32 v162, -v151, v172, v162
	v_fma_f32 v163, -v151, v173, v163
	v_mov_b32_e32 v166, v190
	v_mov_b32_e32 v167, v174
	v_fma_f32 v162, -v153, v166, v162
	v_fma_f32 v163, -v153, v167, v163
	v_mov_b32_e32 v174, v191
	v_fma_f32 v162, -v154, v174, v162
	v_fma_f32 v163, -v154, v175, v163
	v_mov_b32_e32 v166, v192
	v_mov_b32_e32 v167, v180
	v_fma_f32 v162, -v157, v166, v162
	v_fma_f32 v163, -v157, v167, v163
	v_mov_b32_e32 v180, v193
	v_fma_f32 v162, -v159, v180, v162
	v_fma_f32 v163, -v159, v181, v163
	v_mov_b32_e32 v166, v194
	v_mov_b32_e32 v167, v182
	v_fma_f32 v162, -v197, v166, v162
	v_fma_f32 v163, -v197, v167, v163
	v_mov_b32_e32 v182, v195
	v_mov_b32_e32 v188, v201
	v_fma_f32 v190, -v182, v188, v162
	v_fma_f32 v191, -v183, v188, v163
	v_fma_f32 v135, -v197, v164, v196
	v_fma_f32 v193, -v130, v191, v190
	v_mov_b32_e32 v192, v191
	v_mov_b32_e32 v162, v201
	v_mov_b32_e32 v163, v191
	v_mov_b32_e32 v164, v165
	s_waitcnt lgkmcnt(0)
	v_mov_b32_e32 v165, v184
	v_mul_f32_e32 v132, v132, v192
	v_mul_f32_e32 v133, v133, v193
	v_mul_f32_e32 v162, v162, v164
	v_mul_f32_e32 v163, v163, v165
	v_sub_f32_e32 v131, v131, v132
	v_sub_f32_e32 v132, v135, v162
	v_sub_f32_e32 v135, v132, v163
	v_sub_f32_e32 v133, v131, v133
	v_mov_b32_e32 v162, v185
	v_mov_b32_e32 v163, v186
	v_mov_b32_e32 v132, v193
	v_mul_f32_e32 v162, v162, v132
	v_mul_f32_e32 v163, v163, v133
	v_cmp_eq_u32_e32 vcc, 12, v144
	v_sub_f32_e32 v131, v135, v162
	v_sub_f32_e32 v192, v131, v163
	ds_read_b128 v[162:165], v179 offset:15328
	ds_read_b128 v[166:169], v179 offset:15344
	ds_read_b128 v[170:173], v179 offset:15104
	ds_read_b128 v[174:177], v179 offset:15120
	ds_read_b128 v[180:183], v179 offset:15136
	v_cndmask_b32_e64 v147, 0, 1.0, vcc
	v_mov_b32_e32 v184, v140
	s_waitcnt lgkmcnt(2)
	v_mov_b32_e32 v185, v170
	v_fma_f32 v146, -v148, v184, v146
	v_fma_f32 v147, -v148, v185, v147
	v_mov_b32_e32 v170, v141
	v_fma_f32 v140, -v151, v170, v146
	v_fma_f32 v141, -v151, v171, v147
	v_mov_b32_e32 v146, v142
	v_mov_b32_e32 v147, v172
	v_fma_f32 v140, -v146, v153, v140
	v_fma_f32 v141, -v147, v153, v141
	v_mov_b32_e32 v172, v143
	v_fma_f32 v140, -v172, v154, v140
	v_fma_f32 v141, -v173, v154, v141
	v_mov_b32_e32 v142, v136
	s_waitcnt lgkmcnt(1)
	v_mov_b32_e32 v143, v174
	v_fma_f32 v140, -v157, v142, v140
	v_fma_f32 v141, -v157, v143, v141
	v_mov_b32_e32 v174, v137
	v_fma_f32 v136, -v159, v174, v140
	v_fma_f32 v137, -v159, v175, v141
	v_mov_b32_e32 v140, v138
	v_mov_b32_e32 v141, v176
	v_fma_f32 v136, -v140, v197, v136
	v_fma_f32 v137, -v141, v197, v137
	v_mov_b32_e32 v176, v139
	v_fma_f32 v140, -v176, v188, v136
	v_fma_f32 v141, -v177, v188, v137
	v_mov_b32_e32 v142, v162
	s_waitcnt lgkmcnt(0)
	v_mov_b32_e32 v143, v180
	v_fma_f32 v140, -v142, v191, v140
	v_fma_f32 v141, -v143, v191, v141
	v_mov_b32_e32 v180, v163
	v_fma_f32 v140, -v180, v132, v140
	v_fma_f32 v141, -v181, v132, v141
	v_mov_b32_e32 v142, v164
	v_mov_b32_e32 v143, v182
	v_mov_b32_e32 v146, v133
	v_fma_f32 v140, -v142, v146, v140
	v_fma_f32 v141, -v143, v146, v141
	v_mov_b32_e32 v182, v165
	ds_read_b128 v[136:139], v179 offset:15168
	v_fma_f32 v194, -v182, v192, v140
	v_fma_f32 v195, -v183, v192, v141
	ds_read_b128 v[140:143], v179 offset:15184
	ds_read_b128 v[162:165], v179 offset:15200
	ds_read_b128 v[170:173], v179 offset:15232
	v_cmp_eq_u32_e32 vcc, 13, v144
	ds_read_b128 v[174:177], v179 offset:15248
	s_waitcnt lgkmcnt(4)
	v_mov_b32_e32 v183, v136
	v_cndmask_b32_e64 v181, 0, 1.0, vcc
	v_cmp_eq_u32_e32 vcc, 14, v144
	s_waitcnt lgkmcnt(1)
	v_mov_b32_e32 v182, v170
	v_mov_b32_e32 v136, v171
	v_cndmask_b32_e64 v180, 0, 1.0, vcc
	v_fma_f32 v198, -v148, v182, v180
	v_fma_f32 v199, -v148, v183, v181
	v_fma_f32 v136, -v151, v136, v198
	v_fma_f32 v137, -v151, v137, v199
	v_mov_b32_e32 v170, v172
	v_mov_b32_e32 v171, v138
	v_fma_f32 v136, -v153, v170, v136
	v_fma_f32 v137, -v153, v171, v137
	v_mov_b32_e32 v138, v173
	ds_read_b128 v[180:183], v179 offset:15264
	ds_read_b128 v[184:187], v179 offset:15280
	v_fma_f32 v136, -v154, v138, v136
	v_fma_f32 v137, -v154, v139, v137
	s_waitcnt lgkmcnt(2)
	v_mov_b32_e32 v138, v174
	v_mov_b32_e32 v139, v140
	v_fma_f32 v136, -v157, v138, v136
	v_fma_f32 v137, -v157, v139, v137
	v_mov_b32_e32 v140, v175
	v_fma_f32 v136, -v159, v140, v136
	v_fma_f32 v137, -v159, v141, v137
	v_mov_b32_e32 v138, v176
	v_mov_b32_e32 v139, v142
	v_fma_f32 v136, -v197, v138, v136
	v_fma_f32 v137, -v197, v139, v137
	v_mov_b32_e32 v142, v177
	v_fma_f32 v136, -v188, v142, v136
	v_fma_f32 v137, -v188, v143, v137
	s_waitcnt lgkmcnt(1)
	v_mov_b32_e32 v138, v180
	v_mov_b32_e32 v139, v162
	v_fma_f32 v136, -v191, v138, v136
	v_fma_f32 v137, -v191, v139, v137
	v_mov_b32_e32 v162, v181
	v_fma_f32 v136, -v132, v162, v136
	v_fma_f32 v137, -v132, v163, v137
	v_mov_b32_e32 v138, v182
	v_mov_b32_e32 v139, v164
	v_fma_f32 v136, -v146, v138, v136
	v_fma_f32 v137, -v146, v139, v137
	v_mov_b32_e32 v164, v183
	v_fma_f32 v136, -v192, v164, v136
	v_fma_f32 v137, -v192, v165, v137
	s_waitcnt lgkmcnt(0)
	v_mov_b32_e32 v138, v184
	v_mov_b32_e32 v139, v134
	v_fma_f32 v136, -v138, v195, v136
	v_fma_f32 v137, -v139, v195, v137
	v_mov_b32_e32 v138, v167
	v_fma_f32 v135, -v185, v137, v136
	v_mov_b32_e32 v139, v168
	v_mov_b32_e32 v134, v137
	v_cvt_f16_f32_e32 v132, v191
	v_fma_f32 v131, -v166, v195, v194
	v_mul_f32_e32 v138, v138, v134
	v_mul_f32_e32 v139, v139, v135
	v_cvt_pk_f16_f32 v134, v195, v137
	v_sub_f32_e32 v131, v131, v138
	v_sub_f32_e32 v131, v131, v139
	v_cvt_pk_f16_f32 v139, v197, v201
	v_cvt_pk_f16_f32 v138, v157, v159
	v_cvt_pk_f16_f32 v137, v153, v154
	v_cvt_pk_f16_f32 v136, v148, v151
	v_cvt_pk_f16_f32 v135, v135, v131
	v_cvt_pk_f16_f32 v133, v133, v192
	v_fma_mixhi_f16 v132, -v130, v191, v190
	ds_write_b128 v161, v[136:139] offset:15360
	ds_write_b128 v161, v[132:135] offset:15376
	s_branch .LBB0_1289
